# static priority: the s_setprio 0 / s_setprio 1 flip between the two MFMA groups of every compute segment removed in all 8-phase K-loops (40 places); two s_nop placed after the segment's last MFMA keep
# speedup vs baseline: 1.0106x; 1.0083x over previous
.LBB0_357:
	s_and_b64 s[10:11], s[72:73], exec
	s_cselect_b32 s5, s69, s7
	s_cselect_b32 s30, s68, s6
	s_cselect_b32 s31, s71, s9
	s_cselect_b32 s36, s70, s8
	s_add_u32 s6, s6, 0x40080
	s_addc_u32 s7, s7, 0
	s_add_u32 s37, s8, 0x100
	s_addc_u32 s67, s9, 0
	s_mov_b32 s74, -2
	ds_read_b128 v[16:19], v183
	ds_read_b128 v[20:23], v183 offset:1024
	ds_read_b128 v[24:27], v183 offset:2048
	ds_read_b128 v[28:31], v183 offset:3072
	ds_read_b128 v[0:3], v184
	ds_read_b128 v[4:7], v184 offset:1024
	ds_read_b128 v[8:11], v184 offset:2048
	ds_read_b128 v[12:15], v184 offset:3072
	s_add_u32 s8, s6, 0xfffc0080
	s_addc_u32 s9, s7, -1
	s_cmp_eq_u32 s74, 12
	s_cselect_b32 s11, s5, s9
	s_cselect_b32 s10, s30, s8
	s_cselect_b32 s9, s31, s67
	s_cselect_b32 s8, s36, s37
	v_lshl_add_u64 v[212:213], s[6:7], 0, v[170:171]
	s_add_i32 m0, s83, 0xc000
	ds_read_b128 v[174:177], v185
	ds_read_b128 v[178:181], v185 offset:1024
	ds_read_b128 v[188:191], v185 offset:2048
	ds_read_b128 v[192:195], v185 offset:3072
	ds_read_b128 v[196:199], v185 offset:4096
	ds_read_b128 v[200:203], v185 offset:5120
	ds_read_b128 v[204:207], v185 offset:6144
	ds_read_b128 v[208:211], v185 offset:7168
	global_load_lds_dwordx4 v[212:213], off
	v_lshl_add_u64 v[212:213], s[6:7], 0, v[172:173]
	s_add_i32 m0, s83, 0xe000
	s_nop 0
	global_load_lds_dwordx4 v[212:213], off
	s_waitcnt vmcnt(8)
	s_waitcnt lgkmcnt(0)
	s_barrier
	s_setprio 1
	s_waitcnt lgkmcnt(0)
	v_mfma_f32_16x16x128_f8f6f4 v[156:159], v[16:23], v[174:181], 0
	v_mfma_f32_16x16x128_f8f6f4 v[152:155], v[24:31], v[174:181], 0
	v_mfma_f32_16x16x128_f8f6f4 v[140:143], v[16:23], v[188:195], 0
	v_mfma_f32_16x16x128_f8f6f4 v[136:139], v[24:31], v[188:195], 0
	v_mfma_f32_16x16x128_f8f6f4 v[124:127], v[16:23], v[196:203], 0
	v_mfma_f32_16x16x128_f8f6f4 v[120:123], v[24:31], v[196:203], 0
	v_mfma_f32_16x16x128_f8f6f4 v[108:111], v[16:23], v[204:211], 0
	v_mfma_f32_16x16x128_f8f6f4 v[104:107], v[24:31], v[204:211], 0
	v_mfma_f32_16x16x128_f8f6f4 v[148:151], v[0:7], v[174:181], 0
	v_mfma_f32_16x16x128_f8f6f4 v[144:147], v[8:15], v[174:181], 0
	v_mfma_f32_16x16x128_f8f6f4 v[132:135], v[0:7], v[188:195], 0
	v_mfma_f32_16x16x128_f8f6f4 v[128:131], v[8:15], v[188:195], 0
	v_mfma_f32_16x16x128_f8f6f4 v[116:119], v[0:7], v[196:203], 0
	v_mfma_f32_16x16x128_f8f6f4 v[112:115], v[8:15], v[196:203], 0
	v_mfma_f32_16x16x128_f8f6f4 v[100:103], v[0:7], v[204:211], 0
	v_mfma_f32_16x16x128_f8f6f4 v[96:99], v[8:15], v[204:211], 0
	s_setprio 0
	s_nop 0
	s_nop 0
	s_barrier
	s_add_i32 s75, s89, s38
	v_lshl_add_u64 v[174:175], s[8:9], 0, v[162:163]
	s_mov_b32 m0, s75
	ds_read_b128 v[188:191], v185 offset:16384
	ds_read_b128 v[192:195], v185 offset:17408
	ds_read_b128 v[196:199], v185 offset:18432
	ds_read_b128 v[200:203], v185 offset:19456
	ds_read_b128 v[204:207], v185 offset:20480
	ds_read_b128 v[208:211], v185 offset:21504
	ds_read_b128 v[212:215], v185 offset:22528
	ds_read_b128 v[216:219], v185 offset:23552
	global_load_lds_dwordx4 v[174:175], off
	s_add_i32 m0, s75, 0x2000
	s_add_u32 s76, s8, 0x40000
	v_lshl_add_u64 v[176:177], s[8:9], 0, v[166:167]
	s_addc_u32 s77, s9, 0
	s_add_i32 s75, s90, s38
	global_load_lds_dwordx4 v[176:177], off
	v_lshl_add_u64 v[178:179], s[76:77], 0, v[162:163]
	s_mov_b32 m0, s75
	v_lshl_add_u64 v[180:181], s[10:11], 0, v[164:165]
	global_load_lds_dwordx4 v[178:179], off
	v_lshl_add_u64 v[178:179], s[76:77], 0, v[166:167]
	s_add_i32 m0, s75, 0x2000
	s_nop 0
	global_load_lds_dwordx4 v[178:179], off
	v_lshl_add_u64 v[178:179], s[10:11], 0, v[160:161]
	s_mov_b32 m0, s83
	s_nop 0
	global_load_lds_dwordx4 v[178:179], off
	s_mov_b32 m0, s84
	s_nop 0
	global_load_lds_dwordx4 v[180:181], off
	s_waitcnt vmcnt(8)
	s_waitcnt lgkmcnt(0)
	s_barrier
	s_setprio 1
	s_waitcnt lgkmcnt(0)
	v_mfma_f32_16x16x128_f8f6f4 v[92:95], v[16:23], v[188:195], 0
	v_mfma_f32_16x16x128_f8f6f4 v[88:91], v[24:31], v[188:195], 0
	v_mfma_f32_16x16x128_f8f6f4 v[76:79], v[16:23], v[196:203], 0
	v_mfma_f32_16x16x128_f8f6f4 v[72:75], v[24:31], v[196:203], 0
	v_mfma_f32_16x16x128_f8f6f4 v[60:63], v[16:23], v[204:211], 0
	v_mfma_f32_16x16x128_f8f6f4 v[56:59], v[24:31], v[204:211], 0
	v_mfma_f32_16x16x128_f8f6f4 v[44:47], v[16:23], v[212:219], 0
	v_mfma_f32_16x16x128_f8f6f4 v[40:43], v[24:31], v[212:219], 0
	v_mfma_f32_16x16x128_f8f6f4 v[84:87], v[0:7], v[188:195], 0
	v_mfma_f32_16x16x128_f8f6f4 v[80:83], v[8:15], v[188:195], 0
	v_mfma_f32_16x16x128_f8f6f4 v[68:71], v[0:7], v[196:203], 0
	v_mfma_f32_16x16x128_f8f6f4 v[64:67], v[8:15], v[196:203], 0
	v_mfma_f32_16x16x128_f8f6f4 v[52:55], v[0:7], v[204:211], 0
	v_mfma_f32_16x16x128_f8f6f4 v[48:51], v[8:15], v[204:211], 0
	v_mfma_f32_16x16x128_f8f6f4 v[36:39], v[0:7], v[212:219], 0
	v_mfma_f32_16x16x128_f8f6f4 v[32:35], v[8:15], v[212:219], 0
	s_setprio 0
	s_nop 0
	s_nop 0
	s_barrier
	s_branch .Lpeel1f_sub3
.LBB0_358:
	ds_read_b128 v[16:19], v183
	ds_read_b128 v[20:23], v183 offset:1024
	ds_read_b128 v[24:27], v183 offset:2048
	ds_read_b128 v[28:31], v183 offset:3072
	ds_read_b128 v[0:3], v184
	ds_read_b128 v[4:7], v184 offset:1024
	ds_read_b128 v[8:11], v184 offset:2048
	ds_read_b128 v[12:15], v184 offset:3072
	s_add_u32 s8, s6, 0xfffc0080
	s_addc_u32 s9, s7, -1
	s_cmp_eq_u32 s74, 12
	s_cselect_b32 s11, s5, s9
	s_cselect_b32 s10, s30, s8
	s_cselect_b32 s9, s31, s67
	s_cselect_b32 s8, s36, s37
	v_lshl_add_u64 v[212:213], s[6:7], 0, v[170:171]
	s_add_i32 m0, s83, 0xc000
	ds_read_b128 v[174:177], v185
	ds_read_b128 v[178:181], v185 offset:1024
	ds_read_b128 v[188:191], v185 offset:2048
	ds_read_b128 v[192:195], v185 offset:3072
	ds_read_b128 v[196:199], v185 offset:4096
	ds_read_b128 v[200:203], v185 offset:5120
	ds_read_b128 v[204:207], v185 offset:6144
	ds_read_b128 v[208:211], v185 offset:7168
	global_load_lds_dwordx4 v[212:213], off
	v_lshl_add_u64 v[212:213], s[6:7], 0, v[172:173]
	s_add_i32 m0, s83, 0xe000
	s_nop 0
	global_load_lds_dwordx4 v[212:213], off
	s_waitcnt vmcnt(8)
	s_waitcnt lgkmcnt(0)
	s_barrier
	s_setprio 1
	s_waitcnt lgkmcnt(0)
	v_mfma_f32_16x16x128_f8f6f4 v[156:159], v[16:23], v[174:181], v[156:159]
	v_mfma_f32_16x16x128_f8f6f4 v[152:155], v[24:31], v[174:181], v[152:155]
	v_mfma_f32_16x16x128_f8f6f4 v[140:143], v[16:23], v[188:195], v[140:143]
	v_mfma_f32_16x16x128_f8f6f4 v[136:139], v[24:31], v[188:195], v[136:139]
	v_mfma_f32_16x16x128_f8f6f4 v[124:127], v[16:23], v[196:203], v[124:127]
	v_mfma_f32_16x16x128_f8f6f4 v[120:123], v[24:31], v[196:203], v[120:123]
	v_mfma_f32_16x16x128_f8f6f4 v[108:111], v[16:23], v[204:211], v[108:111]
	v_mfma_f32_16x16x128_f8f6f4 v[104:107], v[24:31], v[204:211], v[104:107]
	v_mfma_f32_16x16x128_f8f6f4 v[148:151], v[0:7], v[174:181], v[148:151]
	v_mfma_f32_16x16x128_f8f6f4 v[144:147], v[8:15], v[174:181], v[144:147]
	v_mfma_f32_16x16x128_f8f6f4 v[132:135], v[0:7], v[188:195], v[132:135]
	v_mfma_f32_16x16x128_f8f6f4 v[128:131], v[8:15], v[188:195], v[128:131]
	v_mfma_f32_16x16x128_f8f6f4 v[116:119], v[0:7], v[196:203], v[116:119]
	v_mfma_f32_16x16x128_f8f6f4 v[112:115], v[8:15], v[196:203], v[112:115]
	v_mfma_f32_16x16x128_f8f6f4 v[100:103], v[0:7], v[204:211], v[100:103]
	v_mfma_f32_16x16x128_f8f6f4 v[96:99], v[8:15], v[204:211], v[96:99]
	s_setprio 0
	s_nop 0
	s_nop 0
	s_barrier
	s_add_i32 s75, s89, s38
	v_lshl_add_u64 v[174:175], s[8:9], 0, v[162:163]
	s_mov_b32 m0, s75
	ds_read_b128 v[188:191], v185 offset:16384
	ds_read_b128 v[192:195], v185 offset:17408
	ds_read_b128 v[196:199], v185 offset:18432
	ds_read_b128 v[200:203], v185 offset:19456
	ds_read_b128 v[204:207], v185 offset:20480
	ds_read_b128 v[208:211], v185 offset:21504
	ds_read_b128 v[212:215], v185 offset:22528
	ds_read_b128 v[216:219], v185 offset:23552
	global_load_lds_dwordx4 v[174:175], off
	s_add_i32 m0, s75, 0x2000
	s_add_u32 s76, s8, 0x40000
	v_lshl_add_u64 v[176:177], s[8:9], 0, v[166:167]
	s_addc_u32 s77, s9, 0
	s_add_i32 s75, s90, s38
	global_load_lds_dwordx4 v[176:177], off
	v_lshl_add_u64 v[178:179], s[76:77], 0, v[162:163]
	s_mov_b32 m0, s75
	v_lshl_add_u64 v[180:181], s[10:11], 0, v[164:165]
	global_load_lds_dwordx4 v[178:179], off
	v_lshl_add_u64 v[178:179], s[76:77], 0, v[166:167]
	s_add_i32 m0, s75, 0x2000
	s_nop 0
	global_load_lds_dwordx4 v[178:179], off
	v_lshl_add_u64 v[178:179], s[10:11], 0, v[160:161]
	s_mov_b32 m0, s83
	s_nop 0
	global_load_lds_dwordx4 v[178:179], off
	s_mov_b32 m0, s84
	s_nop 0
	global_load_lds_dwordx4 v[180:181], off
	s_waitcnt vmcnt(8)
	s_waitcnt lgkmcnt(0)
	s_barrier
	s_setprio 1
	s_waitcnt lgkmcnt(0)
	v_mfma_f32_16x16x128_f8f6f4 v[92:95], v[16:23], v[188:195], v[92:95]
	v_mfma_f32_16x16x128_f8f6f4 v[88:91], v[24:31], v[188:195], v[88:91]
	v_mfma_f32_16x16x128_f8f6f4 v[76:79], v[16:23], v[196:203], v[76:79]
	v_mfma_f32_16x16x128_f8f6f4 v[72:75], v[24:31], v[196:203], v[72:75]
	v_mfma_f32_16x16x128_f8f6f4 v[60:63], v[16:23], v[204:211], v[60:63]
	v_mfma_f32_16x16x128_f8f6f4 v[56:59], v[24:31], v[204:211], v[56:59]
	v_mfma_f32_16x16x128_f8f6f4 v[44:47], v[16:23], v[212:219], v[44:47]
	v_mfma_f32_16x16x128_f8f6f4 v[40:43], v[24:31], v[212:219], v[40:43]
	v_mfma_f32_16x16x128_f8f6f4 v[84:87], v[0:7], v[188:195], v[84:87]
	v_mfma_f32_16x16x128_f8f6f4 v[80:83], v[8:15], v[188:195], v[80:83]
	v_mfma_f32_16x16x128_f8f6f4 v[68:71], v[0:7], v[196:203], v[68:71]
	v_mfma_f32_16x16x128_f8f6f4 v[64:67], v[8:15], v[196:203], v[64:67]
	v_mfma_f32_16x16x128_f8f6f4 v[52:55], v[0:7], v[204:211], v[52:55]
	v_mfma_f32_16x16x128_f8f6f4 v[48:51], v[8:15], v[204:211], v[48:51]
	v_mfma_f32_16x16x128_f8f6f4 v[36:39], v[0:7], v[212:219], v[36:39]
	v_mfma_f32_16x16x128_f8f6f4 v[32:35], v[8:15], v[212:219], v[32:35]
	s_setprio 0
	s_nop 0
	s_nop 0
	s_barrier
.Lpeel1f_sub3:
	s_add_i32 s75, 0, 0x18000
	s_add_i32 s76, 0, 0x1c000
	v_add_u32_e32 v12, s75, v182
	v_add_u32_e32 v28, s76, v182
	ds_read_b128 v[0:3], v12
	ds_read_b128 v[4:7], v12 offset:1024
	ds_read_b128 v[8:11], v12 offset:2048
	ds_read_b128 v[12:15], v12 offset:3072
	ds_read_b128 v[16:19], v28
	ds_read_b128 v[20:23], v28 offset:1024
	ds_read_b128 v[24:27], v28 offset:2048
	ds_read_b128 v[28:31], v28 offset:3072
	s_add_u32 s10, s10, 0x40000
	s_addc_u32 s11, s11, 0
	s_mov_b32 m0, s85
	v_lshl_add_u64 v[220:221], s[10:11], 0, v[160:161]
	ds_read_b128 v[188:191], v185 offset:32768
	ds_read_b128 v[192:195], v185 offset:33792
	ds_read_b128 v[196:199], v185 offset:34816
	ds_read_b128 v[200:203], v185 offset:35840
	ds_read_b128 v[204:207], v185 offset:36864
	ds_read_b128 v[208:211], v185 offset:37888
	ds_read_b128 v[212:215], v185 offset:38912
	ds_read_b128 v[216:219], v185 offset:39936
	global_load_lds_dwordx4 v[220:221], off
	v_lshl_add_u64 v[220:221], s[10:11], 0, v[164:165]
	s_mov_b32 m0, s86
	s_nop 0
	global_load_lds_dwordx4 v[220:221], off
	s_waitcnt vmcnt(8)
	s_waitcnt lgkmcnt(0)
	s_barrier
	s_setprio 1
	s_waitcnt lgkmcnt(0)
	v_mfma_f32_16x16x128_f8f6f4 v[156:159], v[0:7], v[188:195], v[156:159]
	v_mfma_f32_16x16x128_f8f6f4 v[152:155], v[8:15], v[188:195], v[152:155]
	v_mfma_f32_16x16x128_f8f6f4 v[140:143], v[0:7], v[196:203], v[140:143]
	v_mfma_f32_16x16x128_f8f6f4 v[136:139], v[8:15], v[196:203], v[136:139]
	v_mfma_f32_16x16x128_f8f6f4 v[124:127], v[0:7], v[204:211], v[124:127]
	v_mfma_f32_16x16x128_f8f6f4 v[120:123], v[8:15], v[204:211], v[120:123]
	v_mfma_f32_16x16x128_f8f6f4 v[108:111], v[0:7], v[212:219], v[108:111]
	v_mfma_f32_16x16x128_f8f6f4 v[104:107], v[8:15], v[212:219], v[104:107]
	v_mfma_f32_16x16x128_f8f6f4 v[148:151], v[16:23], v[188:195], v[148:151]
	v_mfma_f32_16x16x128_f8f6f4 v[144:147], v[24:31], v[188:195], v[144:147]
	v_mfma_f32_16x16x128_f8f6f4 v[132:135], v[16:23], v[196:203], v[132:135]
	v_mfma_f32_16x16x128_f8f6f4 v[128:131], v[24:31], v[196:203], v[128:131]
	v_mfma_f32_16x16x128_f8f6f4 v[116:119], v[16:23], v[204:211], v[116:119]
	v_mfma_f32_16x16x128_f8f6f4 v[112:115], v[24:31], v[204:211], v[112:115]
	v_mfma_f32_16x16x128_f8f6f4 v[100:103], v[16:23], v[212:219], v[100:103]
	v_mfma_f32_16x16x128_f8f6f4 v[96:99], v[24:31], v[212:219], v[96:99]
	s_setprio 0
	s_nop 0
	s_nop 0
	s_barrier
	s_add_i32 s10, s75, s38
	v_lshl_add_u64 v[174:175], v[174:175], 0, s[42:43]
	s_mov_b32 m0, s10
	ds_read_b128 v[188:191], v185 offset:49152
	ds_read_b128 v[192:195], v185 offset:50176
	ds_read_b128 v[196:199], v185 offset:51200
	ds_read_b128 v[200:203], v185 offset:52224
	ds_read_b128 v[204:207], v185 offset:53248
	ds_read_b128 v[208:211], v185 offset:54272
	ds_read_b128 v[212:215], v185 offset:55296
	ds_read_b128 v[216:219], v185 offset:56320
	global_load_lds_dwordx4 v[174:175], off
	s_add_i32 m0, s10, 0x2000
	s_add_u32 s8, s8, 0x40080
	v_lshl_add_u64 v[174:175], v[176:177], 0, s[42:43]
	s_addc_u32 s9, s9, 0
	s_add_i32 s10, s76, s38
	global_load_lds_dwordx4 v[174:175], off
	v_lshl_add_u64 v[174:175], s[8:9], 0, v[162:163]
	s_mov_b32 m0, s10
	s_nop 0
	global_load_lds_dwordx4 v[174:175], off
	v_lshl_add_u64 v[174:175], s[8:9], 0, v[166:167]
	s_add_i32 m0, s10, 0x2000
	s_nop 0
	global_load_lds_dwordx4 v[174:175], off
	v_lshl_add_u64 v[174:175], v[178:179], 0, s[42:43]
	s_mov_b32 m0, s87
	s_nop 0
	global_load_lds_dwordx4 v[174:175], off
	v_lshl_add_u64 v[174:175], v[180:181], 0, s[42:43]
	s_mov_b32 m0, s88
	s_nop 0
	global_load_lds_dwordx4 v[174:175], off
	s_waitcnt vmcnt(8)
	s_waitcnt lgkmcnt(0)
	s_barrier
	s_setprio 1
	s_waitcnt lgkmcnt(0)
	v_mfma_f32_16x16x128_f8f6f4 v[92:95], v[0:7], v[188:195], v[92:95]
	v_mfma_f32_16x16x128_f8f6f4 v[88:91], v[8:15], v[188:195], v[88:91]
	v_mfma_f32_16x16x128_f8f6f4 v[76:79], v[0:7], v[196:203], v[76:79]
	v_mfma_f32_16x16x128_f8f6f4 v[72:75], v[8:15], v[196:203], v[72:75]
	v_mfma_f32_16x16x128_f8f6f4 v[60:63], v[0:7], v[204:211], v[60:63]
	v_mfma_f32_16x16x128_f8f6f4 v[56:59], v[8:15], v[204:211], v[56:59]
	v_mfma_f32_16x16x128_f8f6f4 v[44:47], v[0:7], v[212:219], v[44:47]
	v_mfma_f32_16x16x128_f8f6f4 v[40:43], v[8:15], v[212:219], v[40:43]
	v_mfma_f32_16x16x128_f8f6f4 v[84:87], v[16:23], v[188:195], v[84:87]
	v_mfma_f32_16x16x128_f8f6f4 v[80:83], v[24:31], v[188:195], v[80:83]
	v_mfma_f32_16x16x128_f8f6f4 v[68:71], v[16:23], v[196:203], v[68:71]
	v_mfma_f32_16x16x128_f8f6f4 v[64:67], v[24:31], v[196:203], v[64:67]
	v_mfma_f32_16x16x128_f8f6f4 v[52:55], v[16:23], v[204:211], v[52:55]
	v_mfma_f32_16x16x128_f8f6f4 v[48:51], v[24:31], v[204:211], v[48:51]
	v_mfma_f32_16x16x128_f8f6f4 v[36:39], v[16:23], v[212:219], v[36:39]
	v_mfma_f32_16x16x128_f8f6f4 v[32:35], v[24:31], v[212:219], v[32:35]
	s_setprio 0
	s_nop 0
	s_nop 0
	s_barrier
	s_add_i32 s74, s74, 2
	s_add_u32 s6, s6, 0x100
	s_addc_u32 s7, s7, 0
	s_add_u32 s37, s37, 0x100
	s_addc_u32 s67, s67, 0
	s_cmp_gt_u32 s74, 13
	s_cbranch_scc0 .LBB0_358
	s_and_b64 vcc, exec, s[44:45]
	s_cbranch_vccz .LBB0_361
	s_barrier

.LBB0_510:
	ds_read_b128 v[24:27], v173
	ds_read_b128 v[28:31], v173 offset:1024
	ds_read_b128 v[32:35], v173 offset:2048
	ds_read_b128 v[36:39], v173 offset:3072
	ds_read_b128 v[162:165], v174
	ds_read_b128 v[166:169], v174 offset:1024
	ds_read_b128 v[178:181], v174 offset:2048
	ds_read_b128 v[182:185], v174 offset:3072
	s_add_u32 s8, s6, 0xfff80080
	s_addc_u32 s9, s7, -1
	s_cmp_eq_u32 s65, 28
	s_cselect_b32 s11, s67, s9
	s_cselect_b32 s10, s66, s8
	s_cselect_b32 s9, s69, s63
	s_cselect_b32 s8, s68, s5
	v_lshl_add_u64 v[170:171], s[6:7], 0, v[154:155]
	s_add_i32 m0, s51, 0xc000
	ds_read_b128 v[186:189], v175
	ds_read_b128 v[190:193], v175 offset:1024
	ds_read_b128 v[194:197], v175 offset:2048
	ds_read_b128 v[198:201], v175 offset:3072
	ds_read_b128 v[202:205], v175 offset:4096
	ds_read_b128 v[206:209], v175 offset:5120
	ds_read_b128 v[210:213], v175 offset:6144
	ds_read_b128 v[214:217], v175 offset:7168
	global_load_lds_dwordx4 v[170:171], off
	v_lshl_add_u64 v[170:171], s[6:7], 0, v[156:157]
	s_add_i32 m0, s51, 0xe000
	s_nop 0
	global_load_lds_dwordx4 v[170:171], off
	s_waitcnt vmcnt(8)
	s_waitcnt lgkmcnt(0)
	s_barrier
	s_setprio 1
	s_waitcnt lgkmcnt(0)
	v_mfma_f32_16x16x32_bf16 v[140:143], v[24:27], v[186:189], v[140:143]
	v_mfma_f32_16x16x32_bf16 v[136:139], v[32:35], v[186:189], v[136:139]
	v_mfma_f32_16x16x32_bf16 v[124:127], v[24:27], v[194:197], v[124:127]
	v_mfma_f32_16x16x32_bf16 v[120:123], v[32:35], v[194:197], v[120:123]
	v_mfma_f32_16x16x32_bf16 v[108:111], v[24:27], v[202:205], v[108:111]
	v_mfma_f32_16x16x32_bf16 v[104:107], v[32:35], v[202:205], v[104:107]
	v_mfma_f32_16x16x32_bf16 v[92:95], v[24:27], v[210:213], v[92:95]
	v_mfma_f32_16x16x32_bf16 v[88:91], v[32:35], v[210:213], v[88:91]
	v_mfma_f32_16x16x32_bf16 v[140:143], v[28:31], v[190:193], v[140:143]
	v_mfma_f32_16x16x32_bf16 v[136:139], v[36:39], v[190:193], v[136:139]
	v_mfma_f32_16x16x32_bf16 v[124:127], v[28:31], v[198:201], v[124:127]
	v_mfma_f32_16x16x32_bf16 v[120:123], v[36:39], v[198:201], v[120:123]
	v_mfma_f32_16x16x32_bf16 v[108:111], v[28:31], v[206:209], v[108:111]
	v_mfma_f32_16x16x32_bf16 v[104:107], v[36:39], v[206:209], v[104:107]
	v_mfma_f32_16x16x32_bf16 v[92:95], v[28:31], v[214:217], v[92:95]
	v_mfma_f32_16x16x32_bf16 v[88:91], v[36:39], v[214:217], v[88:91]
	v_mfma_f32_16x16x32_bf16 v[132:135], v[162:165], v[186:189], v[132:135]
	v_mfma_f32_16x16x32_bf16 v[128:131], v[178:181], v[186:189], v[128:131]
	v_mfma_f32_16x16x32_bf16 v[116:119], v[162:165], v[194:197], v[116:119]
	v_mfma_f32_16x16x32_bf16 v[112:115], v[178:181], v[194:197], v[112:115]
	v_mfma_f32_16x16x32_bf16 v[100:103], v[162:165], v[202:205], v[100:103]
	v_mfma_f32_16x16x32_bf16 v[96:99], v[178:181], v[202:205], v[96:99]
	v_mfma_f32_16x16x32_bf16 v[84:87], v[162:165], v[210:213], v[84:87]
	v_mfma_f32_16x16x32_bf16 v[80:83], v[178:181], v[210:213], v[80:83]
	v_mfma_f32_16x16x32_bf16 v[132:135], v[166:169], v[190:193], v[132:135]
	v_mfma_f32_16x16x32_bf16 v[128:131], v[182:185], v[190:193], v[128:131]
	v_mfma_f32_16x16x32_bf16 v[116:119], v[166:169], v[198:201], v[116:119]
	v_mfma_f32_16x16x32_bf16 v[112:115], v[182:185], v[198:201], v[112:115]
	v_mfma_f32_16x16x32_bf16 v[100:103], v[166:169], v[206:209], v[100:103]
	v_mfma_f32_16x16x32_bf16 v[96:99], v[182:185], v[206:209], v[96:99]
	v_mfma_f32_16x16x32_bf16 v[84:87], v[166:169], v[214:217], v[84:87]
	v_mfma_f32_16x16x32_bf16 v[80:83], v[182:185], v[214:217], v[80:83]
	s_setprio 0
	s_nop 0
	s_nop 0
	s_barrier
	s_add_i32 s70, s79, s38
	v_lshl_add_u64 v[170:171], s[8:9], 0, v[146:147]
	s_mov_b32 m0, s70
	ds_read_b128 v[186:189], v175 offset:16384
	ds_read_b128 v[190:193], v175 offset:17408
	ds_read_b128 v[194:197], v175 offset:18432
	ds_read_b128 v[198:201], v175 offset:19456
	ds_read_b128 v[202:205], v175 offset:20480
	ds_read_b128 v[206:209], v175 offset:21504
	ds_read_b128 v[210:213], v175 offset:22528
	ds_read_b128 v[214:217], v175 offset:23552
	global_load_lds_dwordx4 v[170:171], off
	s_add_i32 m0, s70, 0x2000
	s_add_u32 s70, s8, 0x80000
	v_lshl_add_u64 v[218:219], s[8:9], 0, v[150:151]
	s_addc_u32 s71, s9, 0
	s_add_i32 s72, s80, s38
	global_load_lds_dwordx4 v[218:219], off
	v_lshl_add_u64 v[220:221], s[70:71], 0, v[146:147]
	s_mov_b32 m0, s72
	v_lshl_add_u64 v[222:223], s[10:11], 0, v[148:149]
	global_load_lds_dwordx4 v[220:221], off
	v_lshl_add_u64 v[220:221], s[70:71], 0, v[150:151]
	s_add_i32 m0, s72, 0x2000
	s_nop 0
	global_load_lds_dwordx4 v[220:221], off
	v_lshl_add_u64 v[220:221], s[10:11], 0, v[144:145]
	s_mov_b32 m0, s51
	s_nop 0
	global_load_lds_dwordx4 v[220:221], off
	s_mov_b32 m0, s53
	s_nop 0
	global_load_lds_dwordx4 v[222:223], off
	s_waitcnt vmcnt(8)
	s_waitcnt lgkmcnt(0)
	s_barrier
	s_setprio 1
	s_waitcnt lgkmcnt(0)
	v_mfma_f32_16x16x32_bf16 v[76:79], v[24:27], v[186:189], v[76:79]
	v_mfma_f32_16x16x32_bf16 v[72:75], v[32:35], v[186:189], v[72:75]
	v_mfma_f32_16x16x32_bf16 v[60:63], v[24:27], v[194:197], v[60:63]
	v_mfma_f32_16x16x32_bf16 v[56:59], v[32:35], v[194:197], v[56:59]
	v_mfma_f32_16x16x32_bf16 v[44:47], v[24:27], v[202:205], v[44:47]
	v_mfma_f32_16x16x32_bf16 v[40:43], v[32:35], v[202:205], v[40:43]
	v_mfma_f32_16x16x32_bf16 v[12:15], v[24:27], v[210:213], v[12:15]
	v_mfma_f32_16x16x32_bf16 v[8:11], v[32:35], v[210:213], v[8:11]
	v_mfma_f32_16x16x32_bf16 v[76:79], v[28:31], v[190:193], v[76:79]
	v_mfma_f32_16x16x32_bf16 v[72:75], v[36:39], v[190:193], v[72:75]
	v_mfma_f32_16x16x32_bf16 v[60:63], v[28:31], v[198:201], v[60:63]
	v_mfma_f32_16x16x32_bf16 v[56:59], v[36:39], v[198:201], v[56:59]
	v_mfma_f32_16x16x32_bf16 v[44:47], v[28:31], v[206:209], v[44:47]
	v_mfma_f32_16x16x32_bf16 v[40:43], v[36:39], v[206:209], v[40:43]
	v_mfma_f32_16x16x32_bf16 v[12:15], v[28:31], v[214:217], v[12:15]
	v_mfma_f32_16x16x32_bf16 v[8:11], v[36:39], v[214:217], v[8:11]
	v_mfma_f32_16x16x32_bf16 v[20:23], v[162:165], v[202:205], v[20:23]
	v_mfma_f32_16x16x32_bf16 v[16:19], v[178:181], v[202:205], v[16:19]
	v_mfma_f32_16x16x32_bf16 v[4:7], v[162:165], v[210:213], v[4:7]
	v_mfma_f32_16x16x32_bf16 v[0:3], v[178:181], v[210:213], v[0:3]
	v_mfma_f32_16x16x32_bf16 v[24:27], v[162:165], v[186:189], v[68:71]
	v_mfma_f32_16x16x32_bf16 v[28:31], v[178:181], v[186:189], v[64:67]
	v_mfma_f32_16x16x32_bf16 v[32:35], v[162:165], v[194:197], v[52:55]
	v_mfma_f32_16x16x32_bf16 v[36:39], v[178:181], v[194:197], v[48:51]
	v_mfma_f32_16x16x32_bf16 v[20:23], v[166:169], v[206:209], v[20:23]
	v_mfma_f32_16x16x32_bf16 v[16:19], v[182:185], v[206:209], v[16:19]
	v_mfma_f32_16x16x32_bf16 v[4:7], v[166:169], v[214:217], v[4:7]
	v_mfma_f32_16x16x32_bf16 v[0:3], v[182:185], v[214:217], v[0:3]
	v_mfma_f32_16x16x32_bf16 v[24:27], v[166:169], v[190:193], v[24:27]
	v_mfma_f32_16x16x32_bf16 v[28:31], v[182:185], v[190:193], v[28:31]
	v_mfma_f32_16x16x32_bf16 v[32:35], v[166:169], v[198:201], v[32:35]
	v_mfma_f32_16x16x32_bf16 v[36:39], v[182:185], v[198:201], v[36:39]
	s_setprio 0
	s_nop 0
	s_nop 0
	s_barrier
	s_add_i32 s70, 0, 0x18000
	s_add_i32 s71, 0, 0x1c000
	v_add_u32_e32 v68, s70, v172
	v_add_u32_e32 v152, s71, v172
	ds_read_b128 v[48:51], v68
	ds_read_b128 v[52:55], v68 offset:1024
	ds_read_b128 v[64:67], v68 offset:2048
	ds_read_b128 v[68:71], v68 offset:3072
	ds_read_b128 v[162:165], v152
	ds_read_b128 v[166:169], v152 offset:1024
	ds_read_b128 v[178:181], v152 offset:2048
	ds_read_b128 v[182:185], v152 offset:3072
	s_add_u32 s10, s10, 0x80000
	s_addc_u32 s11, s11, 0
	s_mov_b32 m0, s55
	v_lshl_add_u64 v[224:225], s[10:11], 0, v[144:145]
	ds_read_b128 v[186:189], v175 offset:32768
	ds_read_b128 v[190:193], v175 offset:33792
	ds_read_b128 v[194:197], v175 offset:34816
	ds_read_b128 v[198:201], v175 offset:35840
	ds_read_b128 v[202:205], v175 offset:36864
	ds_read_b128 v[206:209], v175 offset:37888
	ds_read_b128 v[210:213], v175 offset:38912
	ds_read_b128 v[214:217], v175 offset:39936
	global_load_lds_dwordx4 v[224:225], off
	v_lshl_add_u64 v[224:225], s[10:11], 0, v[148:149]
	s_mov_b32 m0, s57
	s_nop 0
	global_load_lds_dwordx4 v[224:225], off
	s_waitcnt vmcnt(8)
	s_waitcnt lgkmcnt(0)
	s_barrier
	s_setprio 1
	s_waitcnt lgkmcnt(0)
	v_mfma_f32_16x16x32_bf16 v[140:143], v[48:51], v[186:189], v[140:143]
	v_mfma_f32_16x16x32_bf16 v[136:139], v[64:67], v[186:189], v[136:139]
	v_mfma_f32_16x16x32_bf16 v[124:127], v[48:51], v[194:197], v[124:127]
	v_mfma_f32_16x16x32_bf16 v[120:123], v[64:67], v[194:197], v[120:123]
	v_mfma_f32_16x16x32_bf16 v[108:111], v[48:51], v[202:205], v[108:111]
	v_mfma_f32_16x16x32_bf16 v[104:107], v[64:67], v[202:205], v[104:107]
	v_mfma_f32_16x16x32_bf16 v[92:95], v[48:51], v[210:213], v[92:95]
	v_mfma_f32_16x16x32_bf16 v[88:91], v[64:67], v[210:213], v[88:91]
	v_mfma_f32_16x16x32_bf16 v[140:143], v[52:55], v[190:193], v[140:143]
	v_mfma_f32_16x16x32_bf16 v[136:139], v[68:71], v[190:193], v[136:139]
	v_mfma_f32_16x16x32_bf16 v[124:127], v[52:55], v[198:201], v[124:127]
	v_mfma_f32_16x16x32_bf16 v[120:123], v[68:71], v[198:201], v[120:123]
	v_mfma_f32_16x16x32_bf16 v[108:111], v[52:55], v[206:209], v[108:111]
	v_mfma_f32_16x16x32_bf16 v[104:107], v[68:71], v[206:209], v[104:107]
	v_mfma_f32_16x16x32_bf16 v[92:95], v[52:55], v[214:217], v[92:95]
	v_mfma_f32_16x16x32_bf16 v[88:91], v[68:71], v[214:217], v[88:91]
	v_mfma_f32_16x16x32_bf16 v[132:135], v[162:165], v[186:189], v[132:135]
	v_mfma_f32_16x16x32_bf16 v[128:131], v[178:181], v[186:189], v[128:131]
	v_mfma_f32_16x16x32_bf16 v[116:119], v[162:165], v[194:197], v[116:119]
	v_mfma_f32_16x16x32_bf16 v[112:115], v[178:181], v[194:197], v[112:115]
	v_mfma_f32_16x16x32_bf16 v[100:103], v[162:165], v[202:205], v[100:103]
	v_mfma_f32_16x16x32_bf16 v[96:99], v[178:181], v[202:205], v[96:99]
	v_mfma_f32_16x16x32_bf16 v[84:87], v[162:165], v[210:213], v[84:87]
	v_mfma_f32_16x16x32_bf16 v[80:83], v[178:181], v[210:213], v[80:83]
	v_mfma_f32_16x16x32_bf16 v[132:135], v[166:169], v[190:193], v[132:135]
	v_mfma_f32_16x16x32_bf16 v[128:131], v[182:185], v[190:193], v[128:131]
	v_mfma_f32_16x16x32_bf16 v[116:119], v[166:169], v[198:201], v[116:119]
	v_mfma_f32_16x16x32_bf16 v[112:115], v[182:185], v[198:201], v[112:115]
	v_mfma_f32_16x16x32_bf16 v[100:103], v[166:169], v[206:209], v[100:103]
	v_mfma_f32_16x16x32_bf16 v[96:99], v[182:185], v[206:209], v[96:99]
	v_mfma_f32_16x16x32_bf16 v[84:87], v[166:169], v[214:217], v[84:87]
	v_mfma_f32_16x16x32_bf16 v[80:83], v[182:185], v[214:217], v[80:83]
	s_setprio 0
	s_nop 0
	s_nop 0
	s_barrier
	s_add_i32 s10, s70, s38
	v_lshl_add_u64 v[170:171], v[170:171], 0, s[40:41]
	s_mov_b32 m0, s10
	ds_read_b128 v[186:189], v175 offset:49152
	ds_read_b128 v[190:193], v175 offset:50176
	ds_read_b128 v[194:197], v175 offset:51200
	ds_read_b128 v[198:201], v175 offset:52224
	ds_read_b128 v[202:205], v175 offset:53248
	ds_read_b128 v[206:209], v175 offset:54272
	ds_read_b128 v[210:213], v175 offset:55296
	ds_read_b128 v[214:217], v175 offset:56320
	global_load_lds_dwordx4 v[170:171], off
	s_add_i32 m0, s10, 0x2000
	s_add_u32 s8, s8, 0x80080
	v_lshl_add_u64 v[170:171], v[218:219], 0, s[40:41]
	s_addc_u32 s9, s9, 0
	s_add_i32 s10, s71, s38
	global_load_lds_dwordx4 v[170:171], off
	v_lshl_add_u64 v[170:171], s[8:9], 0, v[146:147]
	s_mov_b32 m0, s10
	s_nop 0
	global_load_lds_dwordx4 v[170:171], off
	v_lshl_add_u64 v[170:171], s[8:9], 0, v[150:151]
	s_add_i32 m0, s10, 0x2000
	s_nop 0
	global_load_lds_dwordx4 v[170:171], off
	v_lshl_add_u64 v[170:171], v[220:221], 0, s[40:41]
	s_mov_b32 m0, s76
	s_nop 0
	global_load_lds_dwordx4 v[170:171], off
	v_lshl_add_u64 v[170:171], v[222:223], 0, s[40:41]
	s_mov_b32 m0, s77
	s_nop 0
	global_load_lds_dwordx4 v[170:171], off
	s_waitcnt vmcnt(8)
	s_waitcnt lgkmcnt(0)
	s_barrier
	s_setprio 1
	s_waitcnt lgkmcnt(0)
	v_mfma_f32_16x16x32_bf16 v[76:79], v[48:51], v[186:189], v[76:79]
	v_mfma_f32_16x16x32_bf16 v[72:75], v[64:67], v[186:189], v[72:75]
	v_mfma_f32_16x16x32_bf16 v[60:63], v[48:51], v[194:197], v[60:63]
	v_mfma_f32_16x16x32_bf16 v[56:59], v[64:67], v[194:197], v[56:59]
	v_mfma_f32_16x16x32_bf16 v[44:47], v[48:51], v[202:205], v[44:47]
	v_mfma_f32_16x16x32_bf16 v[40:43], v[64:67], v[202:205], v[40:43]
	v_mfma_f32_16x16x32_bf16 v[12:15], v[48:51], v[210:213], v[12:15]
	v_mfma_f32_16x16x32_bf16 v[8:11], v[64:67], v[210:213], v[8:11]
	v_mfma_f32_16x16x32_bf16 v[76:79], v[52:55], v[190:193], v[76:79]
	v_mfma_f32_16x16x32_bf16 v[72:75], v[68:71], v[190:193], v[72:75]
	v_mfma_f32_16x16x32_bf16 v[60:63], v[52:55], v[198:201], v[60:63]
	v_mfma_f32_16x16x32_bf16 v[56:59], v[68:71], v[198:201], v[56:59]
	v_mfma_f32_16x16x32_bf16 v[44:47], v[52:55], v[206:209], v[44:47]
	v_mfma_f32_16x16x32_bf16 v[40:43], v[68:71], v[206:209], v[40:43]
	v_mfma_f32_16x16x32_bf16 v[12:15], v[52:55], v[214:217], v[12:15]
	v_mfma_f32_16x16x32_bf16 v[8:11], v[68:71], v[214:217], v[8:11]
	v_mfma_f32_16x16x32_bf16 v[24:27], v[162:165], v[186:189], v[24:27]
	v_mfma_f32_16x16x32_bf16 v[68:71], v[166:169], v[190:193], v[24:27]
	v_mfma_f32_16x16x32_bf16 v[24:27], v[178:181], v[186:189], v[28:31]
	v_mfma_f32_16x16x32_bf16 v[64:67], v[182:185], v[190:193], v[24:27]
	v_mfma_f32_16x16x32_bf16 v[24:27], v[162:165], v[194:197], v[32:35]
	v_mfma_f32_16x16x32_bf16 v[52:55], v[166:169], v[198:201], v[24:27]
	v_mfma_f32_16x16x32_bf16 v[24:27], v[178:181], v[194:197], v[36:39]
	v_mfma_f32_16x16x32_bf16 v[20:23], v[162:165], v[202:205], v[20:23]
	v_mfma_f32_16x16x32_bf16 v[16:19], v[178:181], v[202:205], v[16:19]
	v_mfma_f32_16x16x32_bf16 v[4:7], v[162:165], v[210:213], v[4:7]
	v_mfma_f32_16x16x32_bf16 v[0:3], v[178:181], v[210:213], v[0:3]
	v_mfma_f32_16x16x32_bf16 v[48:51], v[182:185], v[198:201], v[24:27]
	v_mfma_f32_16x16x32_bf16 v[20:23], v[166:169], v[206:209], v[20:23]
	v_mfma_f32_16x16x32_bf16 v[16:19], v[182:185], v[206:209], v[16:19]
	v_mfma_f32_16x16x32_bf16 v[4:7], v[166:169], v[214:217], v[4:7]
	v_mfma_f32_16x16x32_bf16 v[0:3], v[182:185], v[214:217], v[0:3]
	s_setprio 0
	s_nop 0
	s_nop 0
	s_barrier
	s_add_i32 s65, s65, 2
	s_add_u32 s6, s6, 0x100
	s_addc_u32 s7, s7, 0
	s_add_u32 s5, s5, 0x100
	s_addc_u32 s63, s63, 0
	s_cmp_gt_u32 s65, 29
	s_cbranch_scc0 .LBB0_510
	s_and_b64 vcc, exec, s[42:43]
	s_cbranch_vccz .LBB0_513
	s_barrier

.LBB0_858:
	ds_read_b128 v[4:7], v153
	ds_read_b128 v[8:11], v153 offset:1024
	s_waitcnt vmcnt(0)
	ds_read_b128 v[20:23], v153 offset:2048
	ds_read_b128 v[24:27], v153 offset:3072
	ds_read_b128 v[158:161], v154
	ds_read_b128 v[162:165], v154 offset:1024
	ds_read_b128 v[166:169], v154 offset:2048
	ds_read_b128 v[170:173], v154 offset:3072
	s_add_u32 s58, s42, 0x10080
	s_addc_u32 s59, s43, 0
	s_add_i32 s62, s41, 0xc000
	v_lshl_add_u64 v[52:53], s[58:59], 0, v[132:133]
	s_mov_b32 m0, s62
	s_add_i32 s25, s41, 0xe000
	ds_read_b128 v[12:15], v155
	ds_read_b128 v[16:19], v155 offset:1024
	ds_read_b128 v[28:31], v155 offset:2048
	ds_read_b128 v[32:35], v155 offset:3072
	ds_read_b128 v[36:39], v155 offset:4096
	ds_read_b128 v[40:43], v155 offset:5120
	ds_read_b128 v[44:47], v155 offset:6144
	ds_read_b128 v[48:51], v155 offset:7168
	global_load_lds_dwordx4 v[52:53], off
	v_lshl_add_u64 v[52:53], s[58:59], 0, v[136:137]
	s_mov_b32 m0, s25
	s_nop 0
	global_load_lds_dwordx4 v[52:53], off
	s_waitcnt vmcnt(8)
	s_waitcnt lgkmcnt(0)
	s_barrier
	s_setprio 1
	v_mov_b64_e32 v[130:131], v[2:3]
	v_mov_b64_e32 v[126:127], v[2:3]
	v_mov_b64_e32 v[114:115], v[2:3]
	v_mov_b64_e32 v[110:111], v[2:3]
	v_mov_b64_e32 v[98:99], v[2:3]
	v_mov_b64_e32 v[94:95], v[2:3]
	v_mov_b64_e32 v[82:83], v[2:3]
	v_mov_b64_e32 v[78:79], v[2:3]
	v_mov_b64_e32 v[128:129], v[0:1]
	v_mov_b64_e32 v[124:125], v[0:1]
	v_mov_b64_e32 v[112:113], v[0:1]
	v_mov_b64_e32 v[108:109], v[0:1]
	v_mov_b64_e32 v[96:97], v[0:1]
	v_mov_b64_e32 v[92:93], v[0:1]
	v_mov_b64_e32 v[80:81], v[0:1]
	v_mov_b64_e32 v[76:77], v[0:1]
	s_waitcnt lgkmcnt(0)
	v_mfma_f32_16x16x128_f8f6f4 v[128:131], v[4:11], v[12:19], v[128:131]
	v_mfma_f32_16x16x128_f8f6f4 v[124:127], v[20:27], v[12:19], v[124:127]
	v_mfma_f32_16x16x128_f8f6f4 v[112:115], v[4:11], v[28:35], v[112:115]
	v_mfma_f32_16x16x128_f8f6f4 v[108:111], v[20:27], v[28:35], v[108:111]
	v_mfma_f32_16x16x128_f8f6f4 v[96:99], v[4:11], v[36:43], v[96:99]
	v_mfma_f32_16x16x128_f8f6f4 v[92:95], v[20:27], v[36:43], v[92:95]
	v_mfma_f32_16x16x128_f8f6f4 v[80:83], v[4:11], v[44:51], v[80:83]
	v_mfma_f32_16x16x128_f8f6f4 v[76:79], v[20:27], v[44:51], v[76:79]
	s_setprio 0
	s_setprio 1
	v_mov_b64_e32 v[122:123], v[2:3]
	v_mov_b64_e32 v[118:119], v[2:3]
	v_mov_b64_e32 v[106:107], v[2:3]
	v_mov_b64_e32 v[102:103], v[2:3]
	v_mov_b64_e32 v[90:91], v[2:3]
	v_mov_b64_e32 v[86:87], v[2:3]
	v_mov_b64_e32 v[74:75], v[2:3]
	v_mov_b64_e32 v[70:71], v[2:3]
	v_mov_b64_e32 v[120:121], v[0:1]
	v_mov_b64_e32 v[116:117], v[0:1]
	v_mov_b64_e32 v[104:105], v[0:1]
	v_mov_b64_e32 v[100:101], v[0:1]
	v_mov_b64_e32 v[88:89], v[0:1]
	v_mov_b64_e32 v[84:85], v[0:1]
	v_mov_b64_e32 v[72:73], v[0:1]
	v_mov_b64_e32 v[68:69], v[0:1]
	v_mfma_f32_16x16x128_f8f6f4 v[120:123], v[158:165], v[12:19], v[120:123]
	v_mfma_f32_16x16x128_f8f6f4 v[116:119], v[166:173], v[12:19], v[116:119]
	v_mfma_f32_16x16x128_f8f6f4 v[104:107], v[158:165], v[28:35], v[104:107]
	v_mfma_f32_16x16x128_f8f6f4 v[100:103], v[166:173], v[28:35], v[100:103]
	v_mfma_f32_16x16x128_f8f6f4 v[88:91], v[158:165], v[36:43], v[88:91]
	v_mfma_f32_16x16x128_f8f6f4 v[84:87], v[166:173], v[36:43], v[84:87]
	v_mfma_f32_16x16x128_f8f6f4 v[72:75], v[158:165], v[44:51], v[72:75]
	v_mfma_f32_16x16x128_f8f6f4 v[68:71], v[166:173], v[44:51], v[68:71]
	s_setprio 0
	s_barrier
	s_add_i32 s61, s54, s38
	v_lshl_add_u64 v[144:145], s[44:45], 0, v[134:135]
	s_add_i32 s27, s61, 0x2000
	v_lshl_add_u64 v[12:13], v[144:145], 0, s[2:3]
	s_mov_b32 m0, s61
	v_lshl_add_u64 v[146:147], s[44:45], 0, v[138:139]
	s_add_u32 s64, s44, 0x10100
	ds_read_b128 v[36:39], v155 offset:16384
	ds_read_b128 v[40:43], v155 offset:17408
	ds_read_b128 v[174:177], v155 offset:18432
	ds_read_b128 v[178:181], v155 offset:19456
	ds_read_b128 v[182:185], v155 offset:20480
	ds_read_b128 v[186:189], v155 offset:21504
	ds_read_b128 v[190:193], v155 offset:22528
	ds_read_b128 v[194:197], v155 offset:23552
	global_load_lds_dwordx4 v[12:13], off
	v_lshl_add_u64 v[12:13], v[146:147], 0, s[2:3]
	s_mov_b32 m0, s27
	s_addc_u32 s65, s45, 0
	s_add_i32 s58, s55, s38
	global_load_lds_dwordx4 v[12:13], off
	v_lshl_add_u64 v[12:13], s[64:65], 0, v[134:135]
	s_mov_b32 m0, s58
	s_add_i32 s59, s58, 0x2000
	global_load_lds_dwordx4 v[12:13], off
	v_lshl_add_u64 v[12:13], s[64:65], 0, v[138:139]
	s_mov_b32 m0, s59
	v_lshl_add_u64 v[148:149], s[42:43], 0, v[132:133]
	global_load_lds_dwordx4 v[12:13], off
	v_lshl_add_u64 v[12:13], v[148:149], 0, s[2:3]
	s_mov_b32 m0, s41
	v_lshl_add_u64 v[150:151], s[42:43], 0, v[136:137]
	global_load_lds_dwordx4 v[12:13], off
	v_lshl_add_u64 v[12:13], v[150:151], 0, s[2:3]
	s_mov_b32 m0, s48
	s_nop 0
	global_load_lds_dwordx4 v[12:13], off
	s_waitcnt vmcnt(8)
	s_waitcnt lgkmcnt(0)
	s_barrier
	s_setprio 1
	v_mov_b64_e32 v[66:67], v[2:3]
	v_mov_b64_e32 v[62:63], v[2:3]
	v_mov_b64_e32 v[50:51], v[2:3]
	v_mov_b64_e32 v[46:47], v[2:3]
	v_mov_b64_e32 v[34:35], v[2:3]
	v_mov_b64_e32 v[30:31], v[2:3]
	v_mov_b64_e32 v[18:19], v[2:3]
	v_mov_b64_e32 v[14:15], v[2:3]
	v_mov_b64_e32 v[64:65], v[0:1]
	v_mov_b64_e32 v[60:61], v[0:1]
	v_mov_b64_e32 v[48:49], v[0:1]
	v_mov_b64_e32 v[44:45], v[0:1]
	v_mov_b64_e32 v[32:33], v[0:1]
	v_mov_b64_e32 v[28:29], v[0:1]
	v_mov_b64_e32 v[16:17], v[0:1]
	v_mov_b64_e32 v[12:13], v[0:1]
	s_waitcnt lgkmcnt(0)
	v_mfma_f32_16x16x128_f8f6f4 v[64:67], v[4:11], v[36:43], v[64:67]
	v_mfma_f32_16x16x128_f8f6f4 v[60:63], v[20:27], v[36:43], v[60:63]
	v_mfma_f32_16x16x128_f8f6f4 v[48:51], v[4:11], v[174:181], v[48:51]
	v_mfma_f32_16x16x128_f8f6f4 v[44:47], v[20:27], v[174:181], v[44:47]
	v_mfma_f32_16x16x128_f8f6f4 v[32:35], v[4:11], v[182:189], v[32:35]
	v_mfma_f32_16x16x128_f8f6f4 v[28:31], v[20:27], v[182:189], v[28:31]
	v_mfma_f32_16x16x128_f8f6f4 v[16:19], v[4:11], v[190:197], v[16:19]
	v_mfma_f32_16x16x128_f8f6f4 v[12:15], v[20:27], v[190:197], v[12:15]
	s_setprio 0
	s_setprio 1
	v_mov_b64_e32 v[58:59], v[2:3]
	v_mov_b64_e32 v[54:55], v[2:3]
	v_mov_b64_e32 v[56:57], v[0:1]
	v_mov_b64_e32 v[52:53], v[0:1]
	v_mfma_f32_16x16x128_f8f6f4 v[56:59], v[158:165], v[36:43], v[56:59]
	v_mfma_f32_16x16x128_f8f6f4 v[52:55], v[166:173], v[36:43], v[52:55]
	v_mov_b64_e32 v[42:43], v[2:3]
	v_mov_b64_e32 v[38:39], v[2:3]
	v_mov_b64_e32 v[26:27], v[2:3]
	v_mov_b64_e32 v[22:23], v[2:3]
	v_mov_b64_e32 v[10:11], v[2:3]
	v_mov_b64_e32 v[6:7], v[2:3]
	v_mov_b64_e32 v[40:41], v[0:1]
	v_mov_b64_e32 v[36:37], v[0:1]
	v_mov_b64_e32 v[24:25], v[0:1]
	v_mov_b64_e32 v[20:21], v[0:1]
	v_mov_b64_e32 v[8:9], v[0:1]
	v_mov_b64_e32 v[4:5], v[0:1]
	v_mfma_f32_16x16x128_f8f6f4 v[40:43], v[158:165], v[174:181], v[40:43]
	v_mfma_f32_16x16x128_f8f6f4 v[36:39], v[166:173], v[174:181], v[36:39]
	v_mfma_f32_16x16x128_f8f6f4 v[24:27], v[158:165], v[182:189], v[24:27]
	v_mfma_f32_16x16x128_f8f6f4 v[20:23], v[166:173], v[182:189], v[20:23]
	v_mfma_f32_16x16x128_f8f6f4 v[8:11], v[158:165], v[190:197], v[8:11]
	v_mfma_f32_16x16x128_f8f6f4 v[4:7], v[166:173], v[190:197], v[4:7]
	s_setprio 0
	s_barrier
	s_add_i32 s63, 0, 0x18000
	s_add_i32 s66, 0, 0x1c000
	v_add_u32_e32 v157, s63, v152
	v_add_u32_e32 v158, s66, v152
	ds_read_b128 v[160:163], v157
	ds_read_b128 v[164:167], v157 offset:1024
	ds_read_b128 v[168:171], v157 offset:2048
	ds_read_b128 v[172:175], v157 offset:3072
	ds_read_b128 v[176:179], v158
	ds_read_b128 v[180:183], v158 offset:1024
	ds_read_b128 v[184:187], v158 offset:2048
	ds_read_b128 v[188:191], v158 offset:3072
	s_add_u32 s64, s42, 0x10100
	s_addc_u32 s65, s43, 0
	s_mov_b32 m0, s49
	v_lshl_add_u64 v[224:225], s[64:65], 0, v[132:133]
	ds_read_b128 v[192:195], v155 offset:32768
	ds_read_b128 v[196:199], v155 offset:33792
	ds_read_b128 v[200:203], v155 offset:34816
	ds_read_b128 v[204:207], v155 offset:35840
	ds_read_b128 v[208:211], v155 offset:36864
	ds_read_b128 v[212:215], v155 offset:37888
	ds_read_b128 v[216:219], v155 offset:38912
	ds_read_b128 v[220:223], v155 offset:39936
	global_load_lds_dwordx4 v[224:225], off
	v_lshl_add_u64 v[224:225], s[64:65], 0, v[136:137]
	s_mov_b32 m0, s50
	s_nop 0
	global_load_lds_dwordx4 v[224:225], off
	s_waitcnt vmcnt(8)
	s_waitcnt lgkmcnt(0)
	s_barrier
	s_setprio 1
	s_waitcnt lgkmcnt(0)
	v_mfma_f32_16x16x128_f8f6f4 v[128:131], v[160:167], v[192:199], v[128:131]
	v_mfma_f32_16x16x128_f8f6f4 v[124:127], v[168:175], v[192:199], v[124:127]
	v_mfma_f32_16x16x128_f8f6f4 v[112:115], v[160:167], v[200:207], v[112:115]
	v_mfma_f32_16x16x128_f8f6f4 v[108:111], v[168:175], v[200:207], v[108:111]
	v_mfma_f32_16x16x128_f8f6f4 v[96:99], v[160:167], v[208:215], v[96:99]
	v_mfma_f32_16x16x128_f8f6f4 v[92:95], v[168:175], v[208:215], v[92:95]
	v_mfma_f32_16x16x128_f8f6f4 v[80:83], v[160:167], v[216:223], v[80:83]
	v_mfma_f32_16x16x128_f8f6f4 v[76:79], v[168:175], v[216:223], v[76:79]
	v_mfma_f32_16x16x128_f8f6f4 v[120:123], v[176:183], v[192:199], v[120:123]
	v_mfma_f32_16x16x128_f8f6f4 v[116:119], v[184:191], v[192:199], v[116:119]
	v_mfma_f32_16x16x128_f8f6f4 v[104:107], v[176:183], v[200:207], v[104:107]
	v_mfma_f32_16x16x128_f8f6f4 v[100:103], v[184:191], v[200:207], v[100:103]
	v_mfma_f32_16x16x128_f8f6f4 v[88:91], v[176:183], v[208:215], v[88:91]
	v_mfma_f32_16x16x128_f8f6f4 v[84:87], v[184:191], v[208:215], v[84:87]
	v_mfma_f32_16x16x128_f8f6f4 v[72:75], v[176:183], v[216:223], v[72:75]
	v_mfma_f32_16x16x128_f8f6f4 v[68:71], v[184:191], v[216:223], v[68:71]
	s_setprio 0
	s_nop 0
	s_nop 0
	s_barrier
	s_add_i32 s63, s63, s38
	s_add_i32 s60, s63, 0x2000
	v_lshl_add_u64 v[144:145], v[144:145], 0, s[20:21]
	s_mov_b32 m0, s63
	s_add_u32 s64, s44, 0x10180
	ds_read_b128 v[192:195], v155 offset:49152
	ds_read_b128 v[196:199], v155 offset:50176
	ds_read_b128 v[200:203], v155 offset:51200
	ds_read_b128 v[204:207], v155 offset:52224
	ds_read_b128 v[208:211], v155 offset:53248
	ds_read_b128 v[212:215], v155 offset:54272
	ds_read_b128 v[216:219], v155 offset:55296
	ds_read_b128 v[220:223], v155 offset:56320
	global_load_lds_dwordx4 v[144:145], off
	v_lshl_add_u64 v[144:145], v[146:147], 0, s[20:21]
	s_mov_b32 m0, s60
	s_addc_u32 s65, s45, 0
	s_add_i32 s44, s66, s38
	global_load_lds_dwordx4 v[144:145], off
	v_lshl_add_u64 v[144:145], s[64:65], 0, v[134:135]
	s_mov_b32 m0, s44
	s_add_i32 s45, s44, 0x2000
	global_load_lds_dwordx4 v[144:145], off
	v_lshl_add_u64 v[144:145], s[64:65], 0, v[138:139]
	s_mov_b32 m0, s45
	s_nop 0
	global_load_lds_dwordx4 v[144:145], off
	v_lshl_add_u64 v[144:145], v[148:149], 0, s[20:21]
	s_mov_b32 m0, s51
	s_nop 0
	global_load_lds_dwordx4 v[144:145], off
	v_lshl_add_u64 v[144:145], v[150:151], 0, s[20:21]
	s_mov_b32 m0, s52
	s_nop 0
	global_load_lds_dwordx4 v[144:145], off
	s_waitcnt vmcnt(8)
	s_waitcnt lgkmcnt(0)
	s_barrier
	s_setprio 1
	s_waitcnt lgkmcnt(0)
	v_mfma_f32_16x16x128_f8f6f4 v[64:67], v[160:167], v[192:199], v[64:67]
	v_mfma_f32_16x16x128_f8f6f4 v[60:63], v[168:175], v[192:199], v[60:63]
	v_mfma_f32_16x16x128_f8f6f4 v[48:51], v[160:167], v[200:207], v[48:51]
	v_mfma_f32_16x16x128_f8f6f4 v[44:47], v[168:175], v[200:207], v[44:47]
	v_mfma_f32_16x16x128_f8f6f4 v[32:35], v[160:167], v[208:215], v[32:35]
	v_mfma_f32_16x16x128_f8f6f4 v[28:31], v[168:175], v[208:215], v[28:31]
	v_mfma_f32_16x16x128_f8f6f4 v[16:19], v[160:167], v[216:223], v[16:19]
	v_mfma_f32_16x16x128_f8f6f4 v[12:15], v[168:175], v[216:223], v[12:15]
	v_mfma_f32_16x16x128_f8f6f4 v[56:59], v[176:183], v[192:199], v[56:59]
	v_mfma_f32_16x16x128_f8f6f4 v[52:55], v[184:191], v[192:199], v[52:55]
	v_mfma_f32_16x16x128_f8f6f4 v[40:43], v[176:183], v[200:207], v[40:43]
	v_mfma_f32_16x16x128_f8f6f4 v[36:39], v[184:191], v[200:207], v[36:39]
	v_mfma_f32_16x16x128_f8f6f4 v[24:27], v[176:183], v[208:215], v[24:27]
	v_mfma_f32_16x16x128_f8f6f4 v[20:23], v[184:191], v[208:215], v[20:23]
	v_mfma_f32_16x16x128_f8f6f4 v[8:11], v[176:183], v[216:223], v[8:11]
	v_mfma_f32_16x16x128_f8f6f4 v[4:7], v[184:191], v[216:223], v[4:7]
	s_setprio 0
	s_nop 0
	s_nop 0
	s_barrier
	ds_read_b128 v[144:147], v153
	ds_read_b128 v[148:151], v153 offset:1024
	ds_read_b128 v[160:163], v153 offset:2048
	ds_read_b128 v[164:167], v153 offset:3072
	ds_read_b128 v[168:171], v154
	ds_read_b128 v[172:175], v154 offset:1024
	ds_read_b128 v[176:179], v154 offset:2048
	ds_read_b128 v[180:183], v154 offset:3072
	s_add_u32 s42, s42, 0x10180
	s_addc_u32 s43, s43, 0
	s_mov_b32 m0, s62
	v_lshl_add_u64 v[216:217], s[42:43], 0, v[132:133]
	ds_read_b128 v[184:187], v155
	ds_read_b128 v[188:191], v155 offset:1024
	ds_read_b128 v[192:195], v155 offset:2048
	ds_read_b128 v[196:199], v155 offset:3072
	ds_read_b128 v[200:203], v155 offset:4096
	ds_read_b128 v[204:207], v155 offset:5120
	ds_read_b128 v[208:211], v155 offset:6144
	ds_read_b128 v[212:215], v155 offset:7168
	global_load_lds_dwordx4 v[216:217], off
	v_lshl_add_u64 v[216:217], s[42:43], 0, v[136:137]
	s_mov_b32 m0, s25
	s_nop 0
	global_load_lds_dwordx4 v[216:217], off
	s_waitcnt vmcnt(8)
	s_waitcnt lgkmcnt(0)
	s_barrier
	s_setprio 1
	s_waitcnt lgkmcnt(0)
	v_mfma_f32_16x16x128_f8f6f4 v[128:131], v[144:151], v[184:191], v[128:131]
	v_mfma_f32_16x16x128_f8f6f4 v[124:127], v[160:167], v[184:191], v[124:127]
	v_mfma_f32_16x16x128_f8f6f4 v[112:115], v[144:151], v[192:199], v[112:115]
	v_mfma_f32_16x16x128_f8f6f4 v[108:111], v[160:167], v[192:199], v[108:111]
	v_mfma_f32_16x16x128_f8f6f4 v[96:99], v[144:151], v[200:207], v[96:99]
	v_mfma_f32_16x16x128_f8f6f4 v[92:95], v[160:167], v[200:207], v[92:95]
	v_mfma_f32_16x16x128_f8f6f4 v[80:83], v[144:151], v[208:215], v[80:83]
	v_mfma_f32_16x16x128_f8f6f4 v[76:79], v[160:167], v[208:215], v[76:79]
	v_mfma_f32_16x16x128_f8f6f4 v[120:123], v[168:175], v[184:191], v[120:123]
	v_mfma_f32_16x16x128_f8f6f4 v[116:119], v[176:183], v[184:191], v[116:119]
	v_mfma_f32_16x16x128_f8f6f4 v[104:107], v[168:175], v[192:199], v[104:107]
	v_mfma_f32_16x16x128_f8f6f4 v[100:103], v[176:183], v[192:199], v[100:103]
	v_mfma_f32_16x16x128_f8f6f4 v[88:91], v[168:175], v[200:207], v[88:91]
	v_mfma_f32_16x16x128_f8f6f4 v[84:87], v[176:183], v[200:207], v[84:87]
	v_mfma_f32_16x16x128_f8f6f4 v[72:75], v[168:175], v[208:215], v[72:75]
	v_mfma_f32_16x16x128_f8f6f4 v[68:71], v[176:183], v[208:215], v[68:71]
	s_setprio 0
	s_nop 0
	s_nop 0
	s_barrier
	s_mov_b32 m0, s61
	v_lshl_add_u64 v[216:217], s[34:35], 0, v[134:135]
	s_add_u32 s42, s34, 0x10000
	ds_read_b128 v[184:187], v155 offset:16384
	ds_read_b128 v[188:191], v155 offset:17408
	ds_read_b128 v[192:195], v155 offset:18432
	ds_read_b128 v[196:199], v155 offset:19456
	ds_read_b128 v[200:203], v155 offset:20480
	ds_read_b128 v[204:207], v155 offset:21504
	ds_read_b128 v[208:211], v155 offset:22528
	ds_read_b128 v[212:215], v155 offset:23552
	global_load_lds_dwordx4 v[216:217], off
	v_lshl_add_u64 v[218:219], s[34:35], 0, v[138:139]
	s_mov_b32 m0, s27
	s_addc_u32 s43, s35, 0
	global_load_lds_dwordx4 v[218:219], off
	v_lshl_add_u64 v[220:221], s[42:43], 0, v[134:135]
	s_mov_b32 m0, s58
	v_lshl_add_u64 v[222:223], s[28:29], 0, v[136:137]
	global_load_lds_dwordx4 v[220:221], off
	v_lshl_add_u64 v[220:221], s[42:43], 0, v[138:139]
	s_mov_b32 m0, s59
	s_nop 0
	global_load_lds_dwordx4 v[220:221], off
	v_lshl_add_u64 v[220:221], s[28:29], 0, v[132:133]
	s_mov_b32 m0, s41
	s_nop 0
	global_load_lds_dwordx4 v[220:221], off
	s_mov_b32 m0, s48
	s_nop 0
	global_load_lds_dwordx4 v[222:223], off
	s_waitcnt vmcnt(8)
	s_waitcnt lgkmcnt(0)
	s_barrier
	s_setprio 1
	s_waitcnt lgkmcnt(0)
	v_mfma_f32_16x16x128_f8f6f4 v[64:67], v[144:151], v[184:191], v[64:67]
	v_mfma_f32_16x16x128_f8f6f4 v[60:63], v[160:167], v[184:191], v[60:63]
	v_mfma_f32_16x16x128_f8f6f4 v[48:51], v[144:151], v[192:199], v[48:51]
	v_mfma_f32_16x16x128_f8f6f4 v[44:47], v[160:167], v[192:199], v[44:47]
	v_mfma_f32_16x16x128_f8f6f4 v[32:35], v[144:151], v[200:207], v[32:35]
	v_mfma_f32_16x16x128_f8f6f4 v[28:31], v[160:167], v[200:207], v[28:31]
	v_mfma_f32_16x16x128_f8f6f4 v[16:19], v[144:151], v[208:215], v[16:19]
	v_mfma_f32_16x16x128_f8f6f4 v[12:15], v[160:167], v[208:215], v[12:15]
	v_mfma_f32_16x16x128_f8f6f4 v[56:59], v[168:175], v[184:191], v[56:59]
	v_mfma_f32_16x16x128_f8f6f4 v[52:55], v[176:183], v[184:191], v[52:55]
	v_mfma_f32_16x16x128_f8f6f4 v[40:43], v[168:175], v[192:199], v[40:43]
	v_mfma_f32_16x16x128_f8f6f4 v[36:39], v[176:183], v[192:199], v[36:39]
	v_mfma_f32_16x16x128_f8f6f4 v[24:27], v[168:175], v[200:207], v[24:27]
	v_mfma_f32_16x16x128_f8f6f4 v[20:23], v[176:183], v[200:207], v[20:23]
	v_mfma_f32_16x16x128_f8f6f4 v[8:11], v[168:175], v[208:215], v[8:11]
	v_mfma_f32_16x16x128_f8f6f4 v[4:7], v[176:183], v[208:215], v[4:7]
	s_setprio 0
	s_nop 0
	s_nop 0
	s_barrier
	ds_read_b128 v[144:147], v157
	ds_read_b128 v[148:151], v157 offset:1024
	ds_read_b128 v[160:163], v157 offset:2048
	ds_read_b128 v[164:167], v157 offset:3072
	ds_read_b128 v[168:171], v158
	ds_read_b128 v[172:175], v158 offset:1024
	ds_read_b128 v[176:179], v158 offset:2048
	ds_read_b128 v[180:183], v158 offset:3072
	s_add_u32 s42, s28, 0x10000
	s_addc_u32 s43, s29, 0
	s_mov_b32 m0, s49
	v_lshl_add_u64 v[158:159], s[42:43], 0, v[132:133]
	ds_read_b128 v[184:187], v155 offset:32768
	ds_read_b128 v[188:191], v155 offset:33792
	ds_read_b128 v[192:195], v155 offset:34816
	ds_read_b128 v[196:199], v155 offset:35840
	ds_read_b128 v[200:203], v155 offset:36864
	ds_read_b128 v[204:207], v155 offset:37888
	ds_read_b128 v[208:211], v155 offset:38912
	ds_read_b128 v[212:215], v155 offset:39936
	global_load_lds_dwordx4 v[158:159], off
	v_lshl_add_u64 v[158:159], s[42:43], 0, v[136:137]
	s_mov_b32 m0, s50
	s_nop 0
	global_load_lds_dwordx4 v[158:159], off
	s_waitcnt vmcnt(8)
	s_waitcnt lgkmcnt(0)
	s_barrier
	s_setprio 1
	s_waitcnt lgkmcnt(0)
	v_mfma_f32_16x16x128_f8f6f4 v[128:131], v[144:151], v[184:191], v[128:131]
	v_mfma_f32_16x16x128_f8f6f4 v[124:127], v[160:167], v[184:191], v[124:127]
	v_mfma_f32_16x16x128_f8f6f4 v[112:115], v[144:151], v[192:199], v[112:115]
	v_mfma_f32_16x16x128_f8f6f4 v[108:111], v[160:167], v[192:199], v[108:111]
	v_mfma_f32_16x16x128_f8f6f4 v[96:99], v[144:151], v[200:207], v[96:99]
	v_mfma_f32_16x16x128_f8f6f4 v[92:95], v[160:167], v[200:207], v[92:95]
	v_mfma_f32_16x16x128_f8f6f4 v[80:83], v[144:151], v[208:215], v[80:83]
	v_mfma_f32_16x16x128_f8f6f4 v[76:79], v[160:167], v[208:215], v[76:79]
	v_mfma_f32_16x16x128_f8f6f4 v[120:123], v[168:175], v[184:191], v[120:123]
	v_mfma_f32_16x16x128_f8f6f4 v[116:119], v[176:183], v[184:191], v[116:119]
	v_mfma_f32_16x16x128_f8f6f4 v[104:107], v[168:175], v[192:199], v[104:107]
	v_mfma_f32_16x16x128_f8f6f4 v[100:103], v[176:183], v[192:199], v[100:103]
	v_mfma_f32_16x16x128_f8f6f4 v[88:91], v[168:175], v[200:207], v[88:91]
	v_mfma_f32_16x16x128_f8f6f4 v[84:87], v[176:183], v[200:207], v[84:87]
	v_mfma_f32_16x16x128_f8f6f4 v[72:75], v[168:175], v[208:215], v[72:75]
	v_mfma_f32_16x16x128_f8f6f4 v[68:71], v[176:183], v[208:215], v[68:71]
	s_setprio 0
	s_nop 0
	s_nop 0
	s_barrier
	s_mov_b32 m0, s63
	v_lshl_add_u64 v[158:159], v[216:217], 0, s[14:15]
	s_add_u32 s42, s34, 0x10080
	ds_read_b128 v[184:187], v155 offset:49152
	ds_read_b128 v[188:191], v155 offset:50176
	ds_read_b128 v[192:195], v155 offset:51200
	ds_read_b128 v[196:199], v155 offset:52224
	ds_read_b128 v[200:203], v155 offset:53248
	ds_read_b128 v[204:207], v155 offset:54272
	ds_read_b128 v[208:211], v155 offset:55296
	ds_read_b128 v[212:215], v155 offset:56320
	global_load_lds_dwordx4 v[158:159], off
	v_lshl_add_u64 v[158:159], v[218:219], 0, s[14:15]
	s_mov_b32 m0, s60
	s_addc_u32 s43, s35, 0
	global_load_lds_dwordx4 v[158:159], off
	v_lshl_add_u64 v[158:159], s[42:43], 0, v[134:135]
	s_mov_b32 m0, s44
	s_nop 0
	global_load_lds_dwordx4 v[158:159], off
	v_lshl_add_u64 v[158:159], s[42:43], 0, v[138:139]
	s_mov_b32 m0, s45
	s_nop 0
	global_load_lds_dwordx4 v[158:159], off
	v_lshl_add_u64 v[158:159], v[220:221], 0, s[14:15]
	s_mov_b32 m0, s51
	s_nop 0
	global_load_lds_dwordx4 v[158:159], off
	v_lshl_add_u64 v[158:159], v[222:223], 0, s[14:15]
	s_mov_b32 m0, s52
	s_nop 0
	global_load_lds_dwordx4 v[158:159], off
	s_waitcnt vmcnt(8)
	s_waitcnt lgkmcnt(0)
	s_barrier
	s_setprio 1
	s_waitcnt lgkmcnt(0)
	v_mfma_f32_16x16x128_f8f6f4 v[64:67], v[144:151], v[184:191], v[64:67]
	v_mfma_f32_16x16x128_f8f6f4 v[60:63], v[160:167], v[184:191], v[60:63]
	v_mfma_f32_16x16x128_f8f6f4 v[48:51], v[144:151], v[192:199], v[48:51]
	v_mfma_f32_16x16x128_f8f6f4 v[44:47], v[160:167], v[192:199], v[44:47]
	v_mfma_f32_16x16x128_f8f6f4 v[32:35], v[144:151], v[200:207], v[32:35]
	v_mfma_f32_16x16x128_f8f6f4 v[28:31], v[160:167], v[200:207], v[28:31]
	v_mfma_f32_16x16x128_f8f6f4 v[16:19], v[144:151], v[208:215], v[16:19]
	v_mfma_f32_16x16x128_f8f6f4 v[12:15], v[160:167], v[208:215], v[12:15]
	v_mfma_f32_16x16x128_f8f6f4 v[56:59], v[168:175], v[184:191], v[56:59]
	v_mfma_f32_16x16x128_f8f6f4 v[52:55], v[176:183], v[184:191], v[52:55]
	v_mfma_f32_16x16x128_f8f6f4 v[40:43], v[168:175], v[192:199], v[40:43]
	v_mfma_f32_16x16x128_f8f6f4 v[36:39], v[176:183], v[192:199], v[36:39]
	v_mfma_f32_16x16x128_f8f6f4 v[24:27], v[168:175], v[200:207], v[24:27]
	v_mfma_f32_16x16x128_f8f6f4 v[20:23], v[176:183], v[200:207], v[20:23]
	v_mfma_f32_16x16x128_f8f6f4 v[8:11], v[168:175], v[208:215], v[8:11]
	v_mfma_f32_16x16x128_f8f6f4 v[4:7], v[176:183], v[208:215], v[4:7]
	s_setprio 0
	s_nop 0
	s_nop 0
	s_barrier
	s_andn2_b64 vcc, exec, s[16:17]
	s_cbranch_vccnz .LBB0_860
	s_barrier

.LBB0_881:
	ds_read_b128 v[144:147], v151
	ds_read_b128 v[156:159], v151 offset:1024
	ds_read_b128 v[160:163], v151 offset:2048
	ds_read_b128 v[164:167], v151 offset:3072
	ds_read_b128 v[168:171], v152
	ds_read_b128 v[172:175], v152 offset:1024
	ds_read_b128 v[176:179], v152 offset:2048
	ds_read_b128 v[180:183], v152 offset:3072
	s_add_u32 s30, s34, 0xfffc0080
	s_addc_u32 s31, s35, -1
	s_cmp_eq_u32 s56, 12
	s_cselect_b32 s37, s25, s31
	s_cselect_b32 s36, s24, s30
	s_cselect_b32 s31, s27, s23
	s_cselect_b32 s30, s26, s21
	v_lshl_add_u64 v[148:149], s[34:35], 0, v[136:137]
	s_add_i32 m0, s29, 0xc000
	ds_read_b128 v[184:187], v153
	ds_read_b128 v[188:191], v153 offset:1024
	ds_read_b128 v[192:195], v153 offset:2048
	ds_read_b128 v[196:199], v153 offset:3072
	ds_read_b128 v[200:203], v153 offset:4096
	ds_read_b128 v[204:207], v153 offset:5120
	ds_read_b128 v[208:211], v153 offset:6144
	ds_read_b128 v[212:215], v153 offset:7168
	global_load_lds_dwordx4 v[148:149], off
	v_lshl_add_u64 v[148:149], s[34:35], 0, v[138:139]
	s_add_i32 m0, s29, 0xe000
	s_nop 0
	global_load_lds_dwordx4 v[148:149], off
	s_waitcnt vmcnt(8)
	s_waitcnt lgkmcnt(0)
	s_barrier
	s_setprio 1
	s_waitcnt lgkmcnt(0)
	v_mfma_f32_16x16x32_bf16 v[124:127], v[144:147], v[184:187], v[124:127]
	v_mfma_f32_16x16x32_bf16 v[120:123], v[160:163], v[184:187], v[120:123]
	v_mfma_f32_16x16x32_bf16 v[108:111], v[144:147], v[192:195], v[108:111]
	v_mfma_f32_16x16x32_bf16 v[104:107], v[160:163], v[192:195], v[104:107]
	v_mfma_f32_16x16x32_bf16 v[92:95], v[144:147], v[200:203], v[92:95]
	v_mfma_f32_16x16x32_bf16 v[88:91], v[160:163], v[200:203], v[88:91]
	v_mfma_f32_16x16x32_bf16 v[76:79], v[144:147], v[208:211], v[76:79]
	v_mfma_f32_16x16x32_bf16 v[72:75], v[160:163], v[208:211], v[72:75]
	v_mfma_f32_16x16x32_bf16 v[124:127], v[156:159], v[188:191], v[124:127]
	v_mfma_f32_16x16x32_bf16 v[120:123], v[164:167], v[188:191], v[120:123]
	v_mfma_f32_16x16x32_bf16 v[108:111], v[156:159], v[196:199], v[108:111]
	v_mfma_f32_16x16x32_bf16 v[104:107], v[164:167], v[196:199], v[104:107]
	v_mfma_f32_16x16x32_bf16 v[92:95], v[156:159], v[204:207], v[92:95]
	v_mfma_f32_16x16x32_bf16 v[88:91], v[164:167], v[204:207], v[88:91]
	v_mfma_f32_16x16x32_bf16 v[76:79], v[156:159], v[212:215], v[76:79]
	v_mfma_f32_16x16x32_bf16 v[72:75], v[164:167], v[212:215], v[72:75]
	v_mfma_f32_16x16x32_bf16 v[116:119], v[168:171], v[184:187], v[116:119]
	v_mfma_f32_16x16x32_bf16 v[112:115], v[176:179], v[184:187], v[112:115]
	v_mfma_f32_16x16x32_bf16 v[100:103], v[168:171], v[192:195], v[100:103]
	v_mfma_f32_16x16x32_bf16 v[96:99], v[176:179], v[192:195], v[96:99]
	v_mfma_f32_16x16x32_bf16 v[84:87], v[168:171], v[200:203], v[84:87]
	v_mfma_f32_16x16x32_bf16 v[80:83], v[176:179], v[200:203], v[80:83]
	v_mfma_f32_16x16x32_bf16 v[68:71], v[168:171], v[208:211], v[68:71]
	v_mfma_f32_16x16x32_bf16 v[64:67], v[176:179], v[208:211], v[64:67]
	v_mfma_f32_16x16x32_bf16 v[116:119], v[172:175], v[188:191], v[116:119]
	v_mfma_f32_16x16x32_bf16 v[112:115], v[180:183], v[188:191], v[112:115]
	v_mfma_f32_16x16x32_bf16 v[100:103], v[172:175], v[196:199], v[100:103]
	v_mfma_f32_16x16x32_bf16 v[96:99], v[180:183], v[196:199], v[96:99]
	v_mfma_f32_16x16x32_bf16 v[84:87], v[172:175], v[204:207], v[84:87]
	v_mfma_f32_16x16x32_bf16 v[80:83], v[180:183], v[204:207], v[80:83]
	v_mfma_f32_16x16x32_bf16 v[68:71], v[172:175], v[212:215], v[68:71]
	v_mfma_f32_16x16x32_bf16 v[64:67], v[180:183], v[212:215], v[64:67]
	s_setprio 0
	s_nop 0
	s_nop 0
	s_barrier
	s_add_i32 s57, s51, s38
	v_lshl_add_u64 v[148:149], s[30:31], 0, v[130:131]
	s_mov_b32 m0, s57
	ds_read_b128 v[184:187], v153 offset:16384
	ds_read_b128 v[188:191], v153 offset:17408
	ds_read_b128 v[192:195], v153 offset:18432
	ds_read_b128 v[196:199], v153 offset:19456
	ds_read_b128 v[200:203], v153 offset:20480
	ds_read_b128 v[204:207], v153 offset:21504
	ds_read_b128 v[208:211], v153 offset:22528
	ds_read_b128 v[212:215], v153 offset:23552
	global_load_lds_dwordx4 v[148:149], off
	s_add_i32 m0, s57, 0x2000
	s_add_u32 s58, s30, 0x40000
	v_lshl_add_u64 v[216:217], s[30:31], 0, v[134:135]
	s_addc_u32 s59, s31, 0
	s_add_i32 s57, s52, s38
	global_load_lds_dwordx4 v[216:217], off
	v_lshl_add_u64 v[218:219], s[58:59], 0, v[130:131]
	s_mov_b32 m0, s57
	v_lshl_add_u64 v[220:221], s[36:37], 0, v[132:133]
	global_load_lds_dwordx4 v[218:219], off
	v_lshl_add_u64 v[218:219], s[58:59], 0, v[134:135]
	s_add_i32 m0, s57, 0x2000
	s_nop 0
	global_load_lds_dwordx4 v[218:219], off
	v_lshl_add_u64 v[218:219], s[36:37], 0, v[128:129]
	s_mov_b32 m0, s29
	s_nop 0
	global_load_lds_dwordx4 v[218:219], off
	s_mov_b32 m0, s44
	s_nop 0
	global_load_lds_dwordx4 v[220:221], off
	s_waitcnt vmcnt(8)
	s_waitcnt lgkmcnt(0)
	s_barrier
	s_setprio 1
	s_waitcnt lgkmcnt(0)
	v_mfma_f32_16x16x32_bf16 v[60:63], v[144:147], v[184:187], v[60:63]
	v_mfma_f32_16x16x32_bf16 v[56:59], v[160:163], v[184:187], v[56:59]
	v_mfma_f32_16x16x32_bf16 v[44:47], v[144:147], v[192:195], v[44:47]
	v_mfma_f32_16x16x32_bf16 v[40:43], v[160:163], v[192:195], v[40:43]
	v_mfma_f32_16x16x32_bf16 v[28:31], v[144:147], v[200:203], v[28:31]
	v_mfma_f32_16x16x32_bf16 v[24:27], v[160:163], v[200:203], v[24:27]
	v_mfma_f32_16x16x32_bf16 v[12:15], v[144:147], v[208:211], v[12:15]
	v_mfma_f32_16x16x32_bf16 v[8:11], v[160:163], v[208:211], v[8:11]
	v_mfma_f32_16x16x32_bf16 v[60:63], v[156:159], v[188:191], v[60:63]
	v_mfma_f32_16x16x32_bf16 v[56:59], v[164:167], v[188:191], v[56:59]
	v_mfma_f32_16x16x32_bf16 v[44:47], v[156:159], v[196:199], v[44:47]
	v_mfma_f32_16x16x32_bf16 v[40:43], v[164:167], v[196:199], v[40:43]
	v_mfma_f32_16x16x32_bf16 v[28:31], v[156:159], v[204:207], v[28:31]
	v_mfma_f32_16x16x32_bf16 v[24:27], v[164:167], v[204:207], v[24:27]
	v_mfma_f32_16x16x32_bf16 v[12:15], v[156:159], v[212:215], v[12:15]
	v_mfma_f32_16x16x32_bf16 v[8:11], v[164:167], v[212:215], v[8:11]
	v_mfma_f32_16x16x32_bf16 v[52:55], v[168:171], v[184:187], v[52:55]
	v_mfma_f32_16x16x32_bf16 v[48:51], v[176:179], v[184:187], v[48:51]
	v_mfma_f32_16x16x32_bf16 v[36:39], v[168:171], v[192:195], v[36:39]
	v_mfma_f32_16x16x32_bf16 v[32:35], v[176:179], v[192:195], v[32:35]
	v_mfma_f32_16x16x32_bf16 v[20:23], v[168:171], v[200:203], v[20:23]
	v_mfma_f32_16x16x32_bf16 v[16:19], v[176:179], v[200:203], v[16:19]
	v_mfma_f32_16x16x32_bf16 v[4:7], v[168:171], v[208:211], v[4:7]
	v_mfma_f32_16x16x32_bf16 v[0:3], v[176:179], v[208:211], v[0:3]
	v_mfma_f32_16x16x32_bf16 v[52:55], v[172:175], v[188:191], v[52:55]
	v_mfma_f32_16x16x32_bf16 v[48:51], v[180:183], v[188:191], v[48:51]
	v_mfma_f32_16x16x32_bf16 v[36:39], v[172:175], v[196:199], v[36:39]
	v_mfma_f32_16x16x32_bf16 v[32:35], v[180:183], v[196:199], v[32:35]
	v_mfma_f32_16x16x32_bf16 v[20:23], v[172:175], v[204:207], v[20:23]
	v_mfma_f32_16x16x32_bf16 v[16:19], v[180:183], v[204:207], v[16:19]
	v_mfma_f32_16x16x32_bf16 v[4:7], v[172:175], v[212:215], v[4:7]
	v_mfma_f32_16x16x32_bf16 v[0:3], v[180:183], v[212:215], v[0:3]
	s_setprio 0
	s_nop 0
	s_nop 0
	s_barrier
	s_add_i32 s57, 0, 0x18000
	v_add_u32_e32 v155, s57, v150
	s_add_i32 s58, 0, 0x1c000
	ds_read_b128 v[144:147], v155
	ds_read_b128 v[156:159], v155 offset:1024
	ds_read_b128 v[160:163], v155 offset:2048
	ds_read_b128 v[164:167], v155 offset:3072
	v_add_u32_e32 v155, s58, v150
	ds_read_b128 v[168:171], v155
	ds_read_b128 v[172:175], v155 offset:1024
	ds_read_b128 v[176:179], v155 offset:2048
	ds_read_b128 v[180:183], v155 offset:3072
	s_add_u32 s36, s36, 0x40000
	s_addc_u32 s37, s37, 0
	s_mov_b32 m0, s45
	v_lshl_add_u64 v[222:223], s[36:37], 0, v[128:129]
	ds_read_b128 v[184:187], v153 offset:32768
	ds_read_b128 v[188:191], v153 offset:33792
	ds_read_b128 v[192:195], v153 offset:34816
	ds_read_b128 v[196:199], v153 offset:35840
	ds_read_b128 v[200:203], v153 offset:36864
	ds_read_b128 v[204:207], v153 offset:37888
	ds_read_b128 v[208:211], v153 offset:38912
	ds_read_b128 v[212:215], v153 offset:39936
	global_load_lds_dwordx4 v[222:223], off
	v_lshl_add_u64 v[222:223], s[36:37], 0, v[132:133]
	s_mov_b32 m0, s48
	s_nop 0
	global_load_lds_dwordx4 v[222:223], off
	s_waitcnt vmcnt(8)
	s_waitcnt lgkmcnt(0)
	s_barrier
	s_setprio 1
	s_waitcnt lgkmcnt(0)
	v_mfma_f32_16x16x32_bf16 v[124:127], v[144:147], v[184:187], v[124:127]
	v_mfma_f32_16x16x32_bf16 v[120:123], v[160:163], v[184:187], v[120:123]
	v_mfma_f32_16x16x32_bf16 v[108:111], v[144:147], v[192:195], v[108:111]
	v_mfma_f32_16x16x32_bf16 v[104:107], v[160:163], v[192:195], v[104:107]
	v_mfma_f32_16x16x32_bf16 v[92:95], v[144:147], v[200:203], v[92:95]
	v_mfma_f32_16x16x32_bf16 v[88:91], v[160:163], v[200:203], v[88:91]
	v_mfma_f32_16x16x32_bf16 v[76:79], v[144:147], v[208:211], v[76:79]
	v_mfma_f32_16x16x32_bf16 v[72:75], v[160:163], v[208:211], v[72:75]
	v_mfma_f32_16x16x32_bf16 v[124:127], v[156:159], v[188:191], v[124:127]
	v_mfma_f32_16x16x32_bf16 v[120:123], v[164:167], v[188:191], v[120:123]
	v_mfma_f32_16x16x32_bf16 v[108:111], v[156:159], v[196:199], v[108:111]
	v_mfma_f32_16x16x32_bf16 v[104:107], v[164:167], v[196:199], v[104:107]
	v_mfma_f32_16x16x32_bf16 v[92:95], v[156:159], v[204:207], v[92:95]
	v_mfma_f32_16x16x32_bf16 v[88:91], v[164:167], v[204:207], v[88:91]
	v_mfma_f32_16x16x32_bf16 v[76:79], v[156:159], v[212:215], v[76:79]
	v_mfma_f32_16x16x32_bf16 v[72:75], v[164:167], v[212:215], v[72:75]
	v_mfma_f32_16x16x32_bf16 v[116:119], v[168:171], v[184:187], v[116:119]
	v_mfma_f32_16x16x32_bf16 v[112:115], v[176:179], v[184:187], v[112:115]
	v_mfma_f32_16x16x32_bf16 v[100:103], v[168:171], v[192:195], v[100:103]
	v_mfma_f32_16x16x32_bf16 v[96:99], v[176:179], v[192:195], v[96:99]
	v_mfma_f32_16x16x32_bf16 v[84:87], v[168:171], v[200:203], v[84:87]
	v_mfma_f32_16x16x32_bf16 v[80:83], v[176:179], v[200:203], v[80:83]
	v_mfma_f32_16x16x32_bf16 v[68:71], v[168:171], v[208:211], v[68:71]
	v_mfma_f32_16x16x32_bf16 v[64:67], v[176:179], v[208:211], v[64:67]
	v_mfma_f32_16x16x32_bf16 v[116:119], v[172:175], v[188:191], v[116:119]
	v_mfma_f32_16x16x32_bf16 v[112:115], v[180:183], v[188:191], v[112:115]
	v_mfma_f32_16x16x32_bf16 v[100:103], v[172:175], v[196:199], v[100:103]
	v_mfma_f32_16x16x32_bf16 v[96:99], v[180:183], v[196:199], v[96:99]
	v_mfma_f32_16x16x32_bf16 v[84:87], v[172:175], v[204:207], v[84:87]
	v_mfma_f32_16x16x32_bf16 v[80:83], v[180:183], v[204:207], v[80:83]
	v_mfma_f32_16x16x32_bf16 v[68:71], v[172:175], v[212:215], v[68:71]
	v_mfma_f32_16x16x32_bf16 v[64:67], v[180:183], v[212:215], v[64:67]
	s_setprio 0
	s_nop 0
	s_nop 0
	s_barrier
	s_add_i32 s36, s57, s38
	v_lshl_add_u64 v[148:149], v[148:149], 0, s[12:13]
	s_mov_b32 m0, s36
	ds_read_b128 v[184:187], v153 offset:49152
	ds_read_b128 v[188:191], v153 offset:50176
	ds_read_b128 v[192:195], v153 offset:51200
	ds_read_b128 v[196:199], v153 offset:52224
	ds_read_b128 v[200:203], v153 offset:53248
	ds_read_b128 v[204:207], v153 offset:54272
	ds_read_b128 v[208:211], v153 offset:55296
	ds_read_b128 v[212:215], v153 offset:56320
	global_load_lds_dwordx4 v[148:149], off
	s_add_i32 m0, s36, 0x2000
	s_add_u32 s30, s30, 0x40080
	v_lshl_add_u64 v[148:149], v[216:217], 0, s[12:13]
	s_addc_u32 s31, s31, 0
	s_add_i32 s36, s58, s38
	global_load_lds_dwordx4 v[148:149], off
	v_lshl_add_u64 v[148:149], s[30:31], 0, v[130:131]
	s_mov_b32 m0, s36
	s_nop 0
	global_load_lds_dwordx4 v[148:149], off
	v_lshl_add_u64 v[148:149], s[30:31], 0, v[134:135]
	s_add_i32 m0, s36, 0x2000
	s_nop 0
	global_load_lds_dwordx4 v[148:149], off
	v_lshl_add_u64 v[148:149], v[218:219], 0, s[12:13]
	s_mov_b32 m0, s47
	s_nop 0
	global_load_lds_dwordx4 v[148:149], off
	v_lshl_add_u64 v[148:149], v[220:221], 0, s[12:13]
	s_mov_b32 m0, s50
	s_nop 0
	global_load_lds_dwordx4 v[148:149], off
	s_waitcnt vmcnt(8)
	s_waitcnt lgkmcnt(0)
	s_barrier
	s_setprio 1
	s_waitcnt lgkmcnt(0)
	v_mfma_f32_16x16x32_bf16 v[60:63], v[144:147], v[184:187], v[60:63]
	v_mfma_f32_16x16x32_bf16 v[56:59], v[160:163], v[184:187], v[56:59]
	v_mfma_f32_16x16x32_bf16 v[44:47], v[144:147], v[192:195], v[44:47]
	v_mfma_f32_16x16x32_bf16 v[40:43], v[160:163], v[192:195], v[40:43]
	v_mfma_f32_16x16x32_bf16 v[28:31], v[144:147], v[200:203], v[28:31]
	v_mfma_f32_16x16x32_bf16 v[24:27], v[160:163], v[200:203], v[24:27]
	v_mfma_f32_16x16x32_bf16 v[12:15], v[144:147], v[208:211], v[12:15]
	v_mfma_f32_16x16x32_bf16 v[8:11], v[160:163], v[208:211], v[8:11]
	v_mfma_f32_16x16x32_bf16 v[60:63], v[156:159], v[188:191], v[60:63]
	v_mfma_f32_16x16x32_bf16 v[56:59], v[164:167], v[188:191], v[56:59]
	v_mfma_f32_16x16x32_bf16 v[44:47], v[156:159], v[196:199], v[44:47]
	v_mfma_f32_16x16x32_bf16 v[40:43], v[164:167], v[196:199], v[40:43]
	v_mfma_f32_16x16x32_bf16 v[28:31], v[156:159], v[204:207], v[28:31]
	v_mfma_f32_16x16x32_bf16 v[24:27], v[164:167], v[204:207], v[24:27]
	v_mfma_f32_16x16x32_bf16 v[12:15], v[156:159], v[212:215], v[12:15]
	v_mfma_f32_16x16x32_bf16 v[8:11], v[164:167], v[212:215], v[8:11]
	v_mfma_f32_16x16x32_bf16 v[52:55], v[168:171], v[184:187], v[52:55]
	v_mfma_f32_16x16x32_bf16 v[48:51], v[176:179], v[184:187], v[48:51]
	v_mfma_f32_16x16x32_bf16 v[36:39], v[168:171], v[192:195], v[36:39]
	v_mfma_f32_16x16x32_bf16 v[32:35], v[176:179], v[192:195], v[32:35]
	v_mfma_f32_16x16x32_bf16 v[20:23], v[168:171], v[200:203], v[20:23]
	v_mfma_f32_16x16x32_bf16 v[16:19], v[176:179], v[200:203], v[16:19]
	v_mfma_f32_16x16x32_bf16 v[4:7], v[168:171], v[208:211], v[4:7]
	v_mfma_f32_16x16x32_bf16 v[0:3], v[176:179], v[208:211], v[0:3]
	v_mfma_f32_16x16x32_bf16 v[52:55], v[172:175], v[188:191], v[52:55]
	v_mfma_f32_16x16x32_bf16 v[48:51], v[180:183], v[188:191], v[48:51]
	v_mfma_f32_16x16x32_bf16 v[36:39], v[172:175], v[196:199], v[36:39]
	v_mfma_f32_16x16x32_bf16 v[32:35], v[180:183], v[196:199], v[32:35]
	v_mfma_f32_16x16x32_bf16 v[20:23], v[172:175], v[204:207], v[20:23]
	v_mfma_f32_16x16x32_bf16 v[16:19], v[180:183], v[204:207], v[16:19]
	v_mfma_f32_16x16x32_bf16 v[4:7], v[172:175], v[212:215], v[4:7]
	v_mfma_f32_16x16x32_bf16 v[0:3], v[180:183], v[212:215], v[0:3]
	s_setprio 0
	s_nop 0
	s_nop 0
	s_barrier
	s_add_i32 s56, s56, 2
	s_add_u32 s34, s34, 0x100
	s_addc_u32 s35, s35, 0
	s_add_u32 s21, s21, 0x100
	s_addc_u32 s23, s23, 0
	s_cmp_gt_u32 s56, 13
	s_cbranch_scc0 .LBB0_881
	s_and_b64 vcc, exec, s[14:15]
	s_cbranch_vccz .LBB0_884
	s_barrier

.LBB0_957:
	s_add_u32 s42, s30, 0x40080
	s_addc_u32 s43, s31, 0
	s_add_u32 s25, s36, 0x100
	s_addc_u32 s27, s37, 0
	s_mov_b32 s38, -2
	ds_read_b128 v[16:19], v185
	ds_read_b128 v[20:23], v185 offset:1024
	ds_read_b128 v[24:27], v185 offset:2048
	ds_read_b128 v[28:31], v185 offset:3072
	ds_read_b128 v[0:3], v186
	ds_read_b128 v[4:7], v186 offset:1024
	ds_read_b128 v[8:11], v186 offset:2048
	ds_read_b128 v[12:15], v186 offset:3072
	s_add_u32 s30, s42, 0xfffc0080
	s_addc_u32 s31, s43, -1
	s_cmp_eq_u32 s38, 12
	s_cselect_b32 s37, s29, s31
	s_cselect_b32 s36, s28, s30
	s_cselect_b32 s31, s35, s27
	s_cselect_b32 s30, s34, s25
	v_lshl_add_u64 v[212:213], s[42:43], 0, v[168:169]
	s_add_i32 m0, s41, 0xc000
	ds_read_b128 v[176:179], v187
	ds_read_b128 v[180:183], v187 offset:1024
	ds_read_b128 v[188:191], v187 offset:2048
	ds_read_b128 v[192:195], v187 offset:3072
	ds_read_b128 v[196:199], v187 offset:4096
	ds_read_b128 v[200:203], v187 offset:5120
	ds_read_b128 v[204:207], v187 offset:6144
	ds_read_b128 v[208:211], v187 offset:7168
	global_load_lds_dwordx4 v[212:213], off
	v_lshl_add_u64 v[212:213], s[42:43], 0, v[170:171]
	s_add_i32 m0, s41, 0xe000
	s_nop 0
	global_load_lds_dwordx4 v[212:213], off
	s_waitcnt vmcnt(8)
	s_waitcnt lgkmcnt(0)
	s_barrier
	s_setprio 1
	s_waitcnt lgkmcnt(0)
	v_mfma_f32_16x16x128_f8f6f4 v[156:159], v[16:23], v[176:183], 0
	v_mfma_f32_16x16x128_f8f6f4 v[152:155], v[24:31], v[176:183], 0
	v_mfma_f32_16x16x128_f8f6f4 v[140:143], v[16:23], v[188:195], 0
	v_mfma_f32_16x16x128_f8f6f4 v[136:139], v[24:31], v[188:195], 0
	v_mfma_f32_16x16x128_f8f6f4 v[124:127], v[16:23], v[196:203], 0
	v_mfma_f32_16x16x128_f8f6f4 v[120:123], v[24:31], v[196:203], 0
	v_mfma_f32_16x16x128_f8f6f4 v[108:111], v[16:23], v[204:211], 0
	v_mfma_f32_16x16x128_f8f6f4 v[104:107], v[24:31], v[204:211], 0
	v_mfma_f32_16x16x128_f8f6f4 v[148:151], v[0:7], v[176:183], 0
	v_mfma_f32_16x16x128_f8f6f4 v[144:147], v[8:15], v[176:183], 0
	v_mfma_f32_16x16x128_f8f6f4 v[132:135], v[0:7], v[188:195], 0
	v_mfma_f32_16x16x128_f8f6f4 v[128:131], v[8:15], v[188:195], 0
	v_mfma_f32_16x16x128_f8f6f4 v[116:119], v[0:7], v[196:203], 0
	v_mfma_f32_16x16x128_f8f6f4 v[112:115], v[8:15], v[196:203], 0
	v_mfma_f32_16x16x128_f8f6f4 v[100:103], v[0:7], v[204:211], 0
	v_mfma_f32_16x16x128_f8f6f4 v[96:99], v[8:15], v[204:211], 0
	s_setprio 0
	s_nop 0
	s_nop 0
	s_barrier
	s_add_i32 s39, s57, s47
	v_lshl_add_u64 v[176:177], s[30:31], 0, v[162:163]
	s_mov_b32 m0, s39
	ds_read_b128 v[188:191], v187 offset:16384
	ds_read_b128 v[192:195], v187 offset:17408
	ds_read_b128 v[196:199], v187 offset:18432
	ds_read_b128 v[200:203], v187 offset:19456
	ds_read_b128 v[204:207], v187 offset:20480
	ds_read_b128 v[208:211], v187 offset:21504
	ds_read_b128 v[212:215], v187 offset:22528
	ds_read_b128 v[216:219], v187 offset:23552
	global_load_lds_dwordx4 v[176:177], off
	s_add_i32 m0, s39, 0x2000
	s_add_u32 s60, s30, 0x40000
	v_lshl_add_u64 v[178:179], s[30:31], 0, v[166:167]
	s_addc_u32 s61, s31, 0
	s_add_i32 s39, s58, s47
	global_load_lds_dwordx4 v[178:179], off
	v_lshl_add_u64 v[180:181], s[60:61], 0, v[162:163]
	s_mov_b32 m0, s39
	v_lshl_add_u64 v[182:183], s[36:37], 0, v[164:165]
	global_load_lds_dwordx4 v[180:181], off
	v_lshl_add_u64 v[180:181], s[60:61], 0, v[166:167]
	s_add_i32 m0, s39, 0x2000
	s_nop 0
	global_load_lds_dwordx4 v[180:181], off
	v_lshl_add_u64 v[180:181], s[36:37], 0, v[160:161]
	s_mov_b32 m0, s41
	s_nop 0
	global_load_lds_dwordx4 v[180:181], off
	s_mov_b32 m0, s48
	s_nop 0
	global_load_lds_dwordx4 v[182:183], off
	s_waitcnt vmcnt(8)
	s_waitcnt lgkmcnt(0)
	s_barrier
	s_setprio 1
	s_waitcnt lgkmcnt(0)
	v_mfma_f32_16x16x128_f8f6f4 v[92:95], v[16:23], v[188:195], 0
	v_mfma_f32_16x16x128_f8f6f4 v[88:91], v[24:31], v[188:195], 0
	v_mfma_f32_16x16x128_f8f6f4 v[76:79], v[16:23], v[196:203], 0
	v_mfma_f32_16x16x128_f8f6f4 v[72:75], v[24:31], v[196:203], 0
	v_mfma_f32_16x16x128_f8f6f4 v[60:63], v[16:23], v[204:211], 0
	v_mfma_f32_16x16x128_f8f6f4 v[56:59], v[24:31], v[204:211], 0
	v_mfma_f32_16x16x128_f8f6f4 v[44:47], v[16:23], v[212:219], 0
	v_mfma_f32_16x16x128_f8f6f4 v[40:43], v[24:31], v[212:219], 0
	v_mfma_f32_16x16x128_f8f6f4 v[84:87], v[0:7], v[188:195], 0
	v_mfma_f32_16x16x128_f8f6f4 v[80:83], v[8:15], v[188:195], 0
	v_mfma_f32_16x16x128_f8f6f4 v[68:71], v[0:7], v[196:203], 0
	v_mfma_f32_16x16x128_f8f6f4 v[64:67], v[8:15], v[196:203], 0
	v_mfma_f32_16x16x128_f8f6f4 v[52:55], v[0:7], v[204:211], 0
	v_mfma_f32_16x16x128_f8f6f4 v[48:51], v[8:15], v[204:211], 0
	v_mfma_f32_16x16x128_f8f6f4 v[36:39], v[0:7], v[212:219], 0
	v_mfma_f32_16x16x128_f8f6f4 v[32:35], v[8:15], v[212:219], 0
	s_setprio 0
	s_nop 0
	s_nop 0
	s_barrier
	s_branch .Lpeel5_sub3
.LBB0_958:
	ds_read_b128 v[16:19], v185
	ds_read_b128 v[20:23], v185 offset:1024
	ds_read_b128 v[24:27], v185 offset:2048
	ds_read_b128 v[28:31], v185 offset:3072
	ds_read_b128 v[0:3], v186
	ds_read_b128 v[4:7], v186 offset:1024
	ds_read_b128 v[8:11], v186 offset:2048
	ds_read_b128 v[12:15], v186 offset:3072
	s_add_u32 s30, s42, 0xfffc0080
	s_addc_u32 s31, s43, -1
	s_cmp_eq_u32 s38, 12
	s_cselect_b32 s37, s29, s31
	s_cselect_b32 s36, s28, s30
	s_cselect_b32 s31, s35, s27
	s_cselect_b32 s30, s34, s25
	v_lshl_add_u64 v[212:213], s[42:43], 0, v[168:169]
	s_add_i32 m0, s41, 0xc000
	ds_read_b128 v[176:179], v187
	ds_read_b128 v[180:183], v187 offset:1024
	ds_read_b128 v[188:191], v187 offset:2048
	ds_read_b128 v[192:195], v187 offset:3072
	ds_read_b128 v[196:199], v187 offset:4096
	ds_read_b128 v[200:203], v187 offset:5120
	ds_read_b128 v[204:207], v187 offset:6144
	ds_read_b128 v[208:211], v187 offset:7168
	global_load_lds_dwordx4 v[212:213], off
	v_lshl_add_u64 v[212:213], s[42:43], 0, v[170:171]
	s_add_i32 m0, s41, 0xe000
	s_nop 0
	global_load_lds_dwordx4 v[212:213], off
	s_waitcnt vmcnt(8)
	s_waitcnt lgkmcnt(0)
	s_barrier
	s_setprio 1
	s_waitcnt lgkmcnt(0)
	v_mfma_f32_16x16x128_f8f6f4 v[156:159], v[16:23], v[176:183], v[156:159]
	v_mfma_f32_16x16x128_f8f6f4 v[152:155], v[24:31], v[176:183], v[152:155]
	v_mfma_f32_16x16x128_f8f6f4 v[140:143], v[16:23], v[188:195], v[140:143]
	v_mfma_f32_16x16x128_f8f6f4 v[136:139], v[24:31], v[188:195], v[136:139]
	v_mfma_f32_16x16x128_f8f6f4 v[124:127], v[16:23], v[196:203], v[124:127]
	v_mfma_f32_16x16x128_f8f6f4 v[120:123], v[24:31], v[196:203], v[120:123]
	v_mfma_f32_16x16x128_f8f6f4 v[108:111], v[16:23], v[204:211], v[108:111]
	v_mfma_f32_16x16x128_f8f6f4 v[104:107], v[24:31], v[204:211], v[104:107]
	v_mfma_f32_16x16x128_f8f6f4 v[148:151], v[0:7], v[176:183], v[148:151]
	v_mfma_f32_16x16x128_f8f6f4 v[144:147], v[8:15], v[176:183], v[144:147]
	v_mfma_f32_16x16x128_f8f6f4 v[132:135], v[0:7], v[188:195], v[132:135]
	v_mfma_f32_16x16x128_f8f6f4 v[128:131], v[8:15], v[188:195], v[128:131]
	v_mfma_f32_16x16x128_f8f6f4 v[116:119], v[0:7], v[196:203], v[116:119]
	v_mfma_f32_16x16x128_f8f6f4 v[112:115], v[8:15], v[196:203], v[112:115]
	v_mfma_f32_16x16x128_f8f6f4 v[100:103], v[0:7], v[204:211], v[100:103]
	v_mfma_f32_16x16x128_f8f6f4 v[96:99], v[8:15], v[204:211], v[96:99]
	s_setprio 0
	s_nop 0
	s_nop 0
	s_barrier
	s_add_i32 s39, s57, s47
	v_lshl_add_u64 v[176:177], s[30:31], 0, v[162:163]
	s_mov_b32 m0, s39
	ds_read_b128 v[188:191], v187 offset:16384
	ds_read_b128 v[192:195], v187 offset:17408
	ds_read_b128 v[196:199], v187 offset:18432
	ds_read_b128 v[200:203], v187 offset:19456
	ds_read_b128 v[204:207], v187 offset:20480
	ds_read_b128 v[208:211], v187 offset:21504
	ds_read_b128 v[212:215], v187 offset:22528
	ds_read_b128 v[216:219], v187 offset:23552
	global_load_lds_dwordx4 v[176:177], off
	s_add_i32 m0, s39, 0x2000
	s_add_u32 s60, s30, 0x40000
	v_lshl_add_u64 v[178:179], s[30:31], 0, v[166:167]
	s_addc_u32 s61, s31, 0
	s_add_i32 s39, s58, s47
	global_load_lds_dwordx4 v[178:179], off
	v_lshl_add_u64 v[180:181], s[60:61], 0, v[162:163]
	s_mov_b32 m0, s39
	v_lshl_add_u64 v[182:183], s[36:37], 0, v[164:165]
	global_load_lds_dwordx4 v[180:181], off
	v_lshl_add_u64 v[180:181], s[60:61], 0, v[166:167]
	s_add_i32 m0, s39, 0x2000
	s_nop 0
	global_load_lds_dwordx4 v[180:181], off
	v_lshl_add_u64 v[180:181], s[36:37], 0, v[160:161]
	s_mov_b32 m0, s41
	s_nop 0
	global_load_lds_dwordx4 v[180:181], off
	s_mov_b32 m0, s48
	s_nop 0
	global_load_lds_dwordx4 v[182:183], off
	s_waitcnt vmcnt(8)
	s_waitcnt lgkmcnt(0)
	s_barrier
	s_setprio 1
	s_waitcnt lgkmcnt(0)
	v_mfma_f32_16x16x128_f8f6f4 v[92:95], v[16:23], v[188:195], v[92:95]
	v_mfma_f32_16x16x128_f8f6f4 v[88:91], v[24:31], v[188:195], v[88:91]
	v_mfma_f32_16x16x128_f8f6f4 v[76:79], v[16:23], v[196:203], v[76:79]
	v_mfma_f32_16x16x128_f8f6f4 v[72:75], v[24:31], v[196:203], v[72:75]
	v_mfma_f32_16x16x128_f8f6f4 v[60:63], v[16:23], v[204:211], v[60:63]
	v_mfma_f32_16x16x128_f8f6f4 v[56:59], v[24:31], v[204:211], v[56:59]
	v_mfma_f32_16x16x128_f8f6f4 v[44:47], v[16:23], v[212:219], v[44:47]
	v_mfma_f32_16x16x128_f8f6f4 v[40:43], v[24:31], v[212:219], v[40:43]
	v_mfma_f32_16x16x128_f8f6f4 v[84:87], v[0:7], v[188:195], v[84:87]
	v_mfma_f32_16x16x128_f8f6f4 v[80:83], v[8:15], v[188:195], v[80:83]
	v_mfma_f32_16x16x128_f8f6f4 v[68:71], v[0:7], v[196:203], v[68:71]
	v_mfma_f32_16x16x128_f8f6f4 v[64:67], v[8:15], v[196:203], v[64:67]
	v_mfma_f32_16x16x128_f8f6f4 v[52:55], v[0:7], v[204:211], v[52:55]
	v_mfma_f32_16x16x128_f8f6f4 v[48:51], v[8:15], v[204:211], v[48:51]
	v_mfma_f32_16x16x128_f8f6f4 v[36:39], v[0:7], v[212:219], v[36:39]
	v_mfma_f32_16x16x128_f8f6f4 v[32:35], v[8:15], v[212:219], v[32:35]
	s_setprio 0
	s_nop 0
	s_nop 0
	s_barrier
.Lpeel5_sub3:
	s_add_i32 s39, 0, 0x18000
	s_add_i32 s60, 0, 0x1c000
	v_add_u32_e32 v12, s39, v184
	v_add_u32_e32 v28, s60, v184
	ds_read_b128 v[0:3], v12
	ds_read_b128 v[4:7], v12 offset:1024
	ds_read_b128 v[8:11], v12 offset:2048
	ds_read_b128 v[12:15], v12 offset:3072
	ds_read_b128 v[16:19], v28
	ds_read_b128 v[20:23], v28 offset:1024
	ds_read_b128 v[24:27], v28 offset:2048
	ds_read_b128 v[28:31], v28 offset:3072
	s_add_u32 s36, s36, 0x40000
	s_addc_u32 s37, s37, 0
	s_mov_b32 m0, s49
	v_lshl_add_u64 v[220:221], s[36:37], 0, v[160:161]
	ds_read_b128 v[188:191], v187 offset:32768
	ds_read_b128 v[192:195], v187 offset:33792
	ds_read_b128 v[196:199], v187 offset:34816
	ds_read_b128 v[200:203], v187 offset:35840
	ds_read_b128 v[204:207], v187 offset:36864
	ds_read_b128 v[208:211], v187 offset:37888
	ds_read_b128 v[212:215], v187 offset:38912
	ds_read_b128 v[216:219], v187 offset:39936
	global_load_lds_dwordx4 v[220:221], off
	v_lshl_add_u64 v[220:221], s[36:37], 0, v[164:165]
	s_mov_b32 m0, s50
	s_nop 0
	global_load_lds_dwordx4 v[220:221], off
	s_waitcnt vmcnt(8)
	s_waitcnt lgkmcnt(0)
	s_barrier
	s_setprio 1
	s_waitcnt lgkmcnt(0)
	v_mfma_f32_16x16x128_f8f6f4 v[156:159], v[0:7], v[188:195], v[156:159]
	v_mfma_f32_16x16x128_f8f6f4 v[152:155], v[8:15], v[188:195], v[152:155]
	v_mfma_f32_16x16x128_f8f6f4 v[140:143], v[0:7], v[196:203], v[140:143]
	v_mfma_f32_16x16x128_f8f6f4 v[136:139], v[8:15], v[196:203], v[136:139]
	v_mfma_f32_16x16x128_f8f6f4 v[124:127], v[0:7], v[204:211], v[124:127]
	v_mfma_f32_16x16x128_f8f6f4 v[120:123], v[8:15], v[204:211], v[120:123]
	v_mfma_f32_16x16x128_f8f6f4 v[108:111], v[0:7], v[212:219], v[108:111]
	v_mfma_f32_16x16x128_f8f6f4 v[104:107], v[8:15], v[212:219], v[104:107]
	v_mfma_f32_16x16x128_f8f6f4 v[148:151], v[16:23], v[188:195], v[148:151]
	v_mfma_f32_16x16x128_f8f6f4 v[144:147], v[24:31], v[188:195], v[144:147]
	v_mfma_f32_16x16x128_f8f6f4 v[132:135], v[16:23], v[196:203], v[132:135]
	v_mfma_f32_16x16x128_f8f6f4 v[128:131], v[24:31], v[196:203], v[128:131]
	v_mfma_f32_16x16x128_f8f6f4 v[116:119], v[16:23], v[204:211], v[116:119]
	v_mfma_f32_16x16x128_f8f6f4 v[112:115], v[24:31], v[204:211], v[112:115]
	v_mfma_f32_16x16x128_f8f6f4 v[100:103], v[16:23], v[212:219], v[100:103]
	v_mfma_f32_16x16x128_f8f6f4 v[96:99], v[24:31], v[212:219], v[96:99]
	s_setprio 0
	s_nop 0
	s_nop 0
	s_barrier
	s_add_i32 s36, s39, s47
	v_lshl_add_u64 v[176:177], v[176:177], 0, s[10:11]
	s_mov_b32 m0, s36
	ds_read_b128 v[188:191], v187 offset:49152
	ds_read_b128 v[192:195], v187 offset:50176
	ds_read_b128 v[196:199], v187 offset:51200
	ds_read_b128 v[200:203], v187 offset:52224
	ds_read_b128 v[204:207], v187 offset:53248
	ds_read_b128 v[208:211], v187 offset:54272
	ds_read_b128 v[212:215], v187 offset:55296
	ds_read_b128 v[216:219], v187 offset:56320
	global_load_lds_dwordx4 v[176:177], off
	s_add_i32 m0, s36, 0x2000
	s_add_u32 s30, s30, 0x40080
	v_lshl_add_u64 v[176:177], v[178:179], 0, s[10:11]
	s_addc_u32 s31, s31, 0
	s_add_i32 s36, s60, s47
	global_load_lds_dwordx4 v[176:177], off
	v_lshl_add_u64 v[176:177], s[30:31], 0, v[162:163]
	s_mov_b32 m0, s36
	s_nop 0
	global_load_lds_dwordx4 v[176:177], off
	v_lshl_add_u64 v[176:177], s[30:31], 0, v[166:167]
	s_add_i32 m0, s36, 0x2000
	s_nop 0
	global_load_lds_dwordx4 v[176:177], off
	v_lshl_add_u64 v[176:177], v[180:181], 0, s[10:11]
	s_mov_b32 m0, s54
	s_nop 0
	global_load_lds_dwordx4 v[176:177], off
	v_lshl_add_u64 v[176:177], v[182:183], 0, s[10:11]
	s_mov_b32 m0, s55
	s_nop 0
	global_load_lds_dwordx4 v[176:177], off
	s_waitcnt vmcnt(8)
	s_waitcnt lgkmcnt(0)
	s_barrier
	s_setprio 1
	s_waitcnt lgkmcnt(0)
	v_mfma_f32_16x16x128_f8f6f4 v[92:95], v[0:7], v[188:195], v[92:95]
	v_mfma_f32_16x16x128_f8f6f4 v[88:91], v[8:15], v[188:195], v[88:91]
	v_mfma_f32_16x16x128_f8f6f4 v[76:79], v[0:7], v[196:203], v[76:79]
	v_mfma_f32_16x16x128_f8f6f4 v[72:75], v[8:15], v[196:203], v[72:75]
	v_mfma_f32_16x16x128_f8f6f4 v[60:63], v[0:7], v[204:211], v[60:63]
	v_mfma_f32_16x16x128_f8f6f4 v[56:59], v[8:15], v[204:211], v[56:59]
	v_mfma_f32_16x16x128_f8f6f4 v[44:47], v[0:7], v[212:219], v[44:47]
	v_mfma_f32_16x16x128_f8f6f4 v[40:43], v[8:15], v[212:219], v[40:43]
	v_mfma_f32_16x16x128_f8f6f4 v[84:87], v[16:23], v[188:195], v[84:87]
	v_mfma_f32_16x16x128_f8f6f4 v[80:83], v[24:31], v[188:195], v[80:83]
	v_mfma_f32_16x16x128_f8f6f4 v[68:71], v[16:23], v[196:203], v[68:71]
	v_mfma_f32_16x16x128_f8f6f4 v[64:67], v[24:31], v[196:203], v[64:67]
	v_mfma_f32_16x16x128_f8f6f4 v[52:55], v[16:23], v[204:211], v[52:55]
	v_mfma_f32_16x16x128_f8f6f4 v[48:51], v[24:31], v[204:211], v[48:51]
	v_mfma_f32_16x16x128_f8f6f4 v[36:39], v[16:23], v[212:219], v[36:39]
	v_mfma_f32_16x16x128_f8f6f4 v[32:35], v[24:31], v[212:219], v[32:35]
	s_setprio 0
	s_nop 0
	s_nop 0
	s_barrier
	s_add_i32 s38, s38, 2
	s_add_u32 s42, s42, 0x100
	s_addc_u32 s43, s43, 0
	s_add_u32 s25, s25, 0x100
	s_addc_u32 s27, s27, 0
	s_cmp_gt_u32 s38, 13
	s_cbranch_scc0 .LBB0_958
	s_and_b64 vcc, exec, s[12:13]
	s_cbranch_vccz .LBB0_961
	s_barrier

.Lpeel8_cont:
	s_waitcnt vmcnt(8)
	s_add_u32 s36, s34, 0x80
	s_waitcnt lgkmcnt(0)
	s_addc_u32 s37, s35, 0
	s_and_b64 s[30:31], s[30:31], exec
	v_mov_b32_e32 v217, v213
	v_mov_b32_e32 v219, v213
	s_cselect_b32 s37, s7, s37
	s_cselect_b32 s36, s6, s36
	s_cselect_b32 s31, s27, s29
	s_cselect_b32 s30, s26, s23
	s_barrier
	s_setprio 1
	s_waitcnt lgkmcnt(0)
	v_mfma_f32_16x16x128_f8f6f4 v[204:207], v[24:31], v[56:63], 0
	v_mfma_f32_16x16x128_f8f6f4 v[196:199], v[16:23], v[56:63], 0
	v_mfma_f32_16x16x128_f8f6f4 v[188:191], v[24:31], v[48:55], 0
	v_mfma_f32_16x16x128_f8f6f4 v[180:183], v[16:23], v[48:55], 0
	v_mfma_f32_16x16x128_f8f6f4 v[172:175], v[24:31], v[40:47], 0
	v_mfma_f32_16x16x128_f8f6f4 v[164:167], v[16:23], v[40:47], 0
	v_mfma_f32_16x16x128_f8f6f4 v[156:159], v[24:31], v[32:39], 0
	v_mfma_f32_16x16x128_f8f6f4 v[148:151], v[16:23], v[32:39], 0
	v_mfma_f32_16x16x128_f8f6f4 v[200:203], v[8:15], v[56:63], 0
	v_mfma_f32_16x16x128_f8f6f4 v[192:195], v[0:7], v[56:63], 0
	v_mfma_f32_16x16x128_f8f6f4 v[184:187], v[8:15], v[48:55], 0
	v_mfma_f32_16x16x128_f8f6f4 v[176:179], v[0:7], v[48:55], 0
	v_mfma_f32_16x16x128_f8f6f4 v[168:171], v[8:15], v[40:47], 0
	v_mfma_f32_16x16x128_f8f6f4 v[160:163], v[0:7], v[40:47], 0
	v_mfma_f32_16x16x128_f8f6f4 v[152:155], v[8:15], v[32:39], 0
	v_mfma_f32_16x16x128_f8f6f4 v[144:147], v[0:7], v[32:39], 0
	s_setprio 0
	s_nop 0
	s_nop 0
	s_barrier
	s_mov_b32 m0, s40
	v_lshl_add_u64 v[34:35], s[30:31], 0, v[208:209]
	s_add_u32 s64, s30, 0x40000
	ds_read_b128 v[40:43], v237 offset:16384
	ds_read_b128 v[44:47], v237 offset:17408
	ds_read_b128 v[48:51], v237 offset:18432
	ds_read_b128 v[52:55], v237 offset:19456
	ds_read_b128 v[56:59], v237 offset:20480
	ds_read_b128 v[60:63], v237 offset:21504
	ds_read_b128 v[240:243], v237 offset:22528
	ds_read_b128 v[244:247], v237 offset:23552
	global_load_lds_dwordx4 v[34:35], off
	v_lshl_add_u64 v[32:33], s[30:31], 0, v[210:211]
	s_mov_b32 m0, s41
	s_addc_u32 s65, s31, 0
	global_load_lds_dwordx4 v[32:33], off
	v_lshl_add_u64 v[36:37], s[64:65], 0, v[208:209]
	s_mov_b32 m0, s42
	v_mov_b32_e32 v215, v213
	global_load_lds_dwordx4 v[36:37], off
	v_lshl_add_u64 v[36:37], s[64:65], 0, v[210:211]
	s_mov_b32 m0, s43
	v_lshl_add_u64 v[38:39], s[36:37], 0, v[212:213]
	global_load_lds_dwordx4 v[36:37], off
	s_mov_b32 m0, s39
	v_lshl_add_u64 v[36:37], s[36:37], 0, v[214:215]
	global_load_lds_dwordx4 v212, s[36:37]
	s_mov_b32 m0, s44
	s_nop 0
	global_load_lds_dwordx4 v214, s[36:37]
	s_waitcnt vmcnt(8)
	s_waitcnt lgkmcnt(0)
	s_barrier
	s_setprio 1
	s_waitcnt lgkmcnt(0)
	v_mfma_f32_16x16x128_f8f6f4 v[140:143], v[24:31], v[40:47], 0
	v_mfma_f32_16x16x128_f8f6f4 v[132:135], v[16:23], v[40:47], 0
	v_mfma_f32_16x16x128_f8f6f4 v[124:127], v[24:31], v[48:55], 0
	v_mfma_f32_16x16x128_f8f6f4 v[116:119], v[16:23], v[48:55], 0
	v_mfma_f32_16x16x128_f8f6f4 v[108:111], v[24:31], v[56:63], 0
	v_mfma_f32_16x16x128_f8f6f4 v[100:103], v[16:23], v[56:63], 0
	v_mfma_f32_16x16x128_f8f6f4 v[92:95], v[24:31], v[240:247], 0
	v_mfma_f32_16x16x128_f8f6f4 v[84:87], v[16:23], v[240:247], 0
	v_mfma_f32_16x16x128_f8f6f4 v[136:139], v[8:15], v[40:47], 0
	v_mfma_f32_16x16x128_f8f6f4 v[128:131], v[0:7], v[40:47], 0
	v_mfma_f32_16x16x128_f8f6f4 v[120:123], v[8:15], v[48:55], 0
	v_mfma_f32_16x16x128_f8f6f4 v[112:115], v[0:7], v[48:55], 0
	v_mfma_f32_16x16x128_f8f6f4 v[104:107], v[8:15], v[56:63], 0
	v_mfma_f32_16x16x128_f8f6f4 v[96:99], v[0:7], v[56:63], 0
	v_mfma_f32_16x16x128_f8f6f4 v[88:91], v[8:15], v[240:247], 0
	v_mfma_f32_16x16x128_f8f6f4 v[80:83], v[0:7], v[240:247], 0
	s_setprio 0
	s_nop 0
	s_nop 0
	s_barrier
	s_branch .Lpeel8_sub3
.LBB0_1189:
	s_waitcnt vmcnt(8)
	s_add_u32 s36, s34, 0x80
	s_waitcnt lgkmcnt(0)
	s_addc_u32 s37, s35, 0
	s_and_b64 s[30:31], s[30:31], exec
	v_mov_b32_e32 v217, v213
	v_mov_b32_e32 v219, v213
	s_cselect_b32 s37, s7, s37
	s_cselect_b32 s36, s6, s36
	s_cselect_b32 s31, s27, s29
	s_cselect_b32 s30, s26, s23
	s_barrier
	s_setprio 1
	s_waitcnt lgkmcnt(0)
	v_mfma_f32_16x16x128_f8f6f4 v[204:207], v[24:31], v[56:63], v[204:207]
	v_mfma_f32_16x16x128_f8f6f4 v[196:199], v[16:23], v[56:63], v[196:199]
	v_mfma_f32_16x16x128_f8f6f4 v[188:191], v[24:31], v[48:55], v[188:191]
	v_mfma_f32_16x16x128_f8f6f4 v[180:183], v[16:23], v[48:55], v[180:183]
	v_mfma_f32_16x16x128_f8f6f4 v[172:175], v[24:31], v[40:47], v[172:175]
	v_mfma_f32_16x16x128_f8f6f4 v[164:167], v[16:23], v[40:47], v[164:167]
	v_mfma_f32_16x16x128_f8f6f4 v[156:159], v[24:31], v[32:39], v[156:159]
	v_mfma_f32_16x16x128_f8f6f4 v[148:151], v[16:23], v[32:39], v[148:151]
	v_mfma_f32_16x16x128_f8f6f4 v[200:203], v[8:15], v[56:63], v[200:203]
	v_mfma_f32_16x16x128_f8f6f4 v[192:195], v[0:7], v[56:63], v[192:195]
	v_mfma_f32_16x16x128_f8f6f4 v[184:187], v[8:15], v[48:55], v[184:187]
	v_mfma_f32_16x16x128_f8f6f4 v[176:179], v[0:7], v[48:55], v[176:179]
	v_mfma_f32_16x16x128_f8f6f4 v[168:171], v[8:15], v[40:47], v[168:171]
	v_mfma_f32_16x16x128_f8f6f4 v[160:163], v[0:7], v[40:47], v[160:163]
	v_mfma_f32_16x16x128_f8f6f4 v[152:155], v[8:15], v[32:39], v[152:155]
	v_mfma_f32_16x16x128_f8f6f4 v[144:147], v[0:7], v[32:39], v[144:147]
	s_setprio 0
	s_nop 0
	s_nop 0
	s_barrier
	s_mov_b32 m0, s40
	v_lshl_add_u64 v[34:35], s[30:31], 0, v[208:209]
	s_add_u32 s64, s30, 0x40000
	ds_read_b128 v[40:43], v237 offset:16384
	ds_read_b128 v[44:47], v237 offset:17408
	ds_read_b128 v[48:51], v237 offset:18432
	ds_read_b128 v[52:55], v237 offset:19456
	ds_read_b128 v[56:59], v237 offset:20480
	ds_read_b128 v[60:63], v237 offset:21504
	ds_read_b128 v[240:243], v237 offset:22528
	ds_read_b128 v[244:247], v237 offset:23552
	global_load_lds_dwordx4 v[34:35], off
	v_lshl_add_u64 v[32:33], s[30:31], 0, v[210:211]
	s_mov_b32 m0, s41
	s_addc_u32 s65, s31, 0
	global_load_lds_dwordx4 v[32:33], off
	v_lshl_add_u64 v[36:37], s[64:65], 0, v[208:209]
	s_mov_b32 m0, s42
	v_mov_b32_e32 v215, v213
	global_load_lds_dwordx4 v[36:37], off
	v_lshl_add_u64 v[36:37], s[64:65], 0, v[210:211]
	s_mov_b32 m0, s43
	v_lshl_add_u64 v[38:39], s[36:37], 0, v[212:213]
	global_load_lds_dwordx4 v[36:37], off
	s_mov_b32 m0, s39
	v_lshl_add_u64 v[36:37], s[36:37], 0, v[214:215]
	global_load_lds_dwordx4 v212, s[36:37]
	s_mov_b32 m0, s44
	s_nop 0
	global_load_lds_dwordx4 v214, s[36:37]
	s_waitcnt vmcnt(8)
	s_waitcnt lgkmcnt(0)
	s_barrier
	s_setprio 1
	s_waitcnt lgkmcnt(0)
	v_mfma_f32_16x16x128_f8f6f4 v[140:143], v[24:31], v[40:47], v[140:143]
	v_mfma_f32_16x16x128_f8f6f4 v[132:135], v[16:23], v[40:47], v[132:135]
	v_mfma_f32_16x16x128_f8f6f4 v[124:127], v[24:31], v[48:55], v[124:127]
	v_mfma_f32_16x16x128_f8f6f4 v[116:119], v[16:23], v[48:55], v[116:119]
	v_mfma_f32_16x16x128_f8f6f4 v[108:111], v[24:31], v[56:63], v[108:111]
	v_mfma_f32_16x16x128_f8f6f4 v[100:103], v[16:23], v[56:63], v[100:103]
	v_mfma_f32_16x16x128_f8f6f4 v[92:95], v[24:31], v[240:247], v[92:95]
	v_mfma_f32_16x16x128_f8f6f4 v[84:87], v[16:23], v[240:247], v[84:87]
	v_mfma_f32_16x16x128_f8f6f4 v[136:139], v[8:15], v[40:47], v[136:139]
	v_mfma_f32_16x16x128_f8f6f4 v[128:131], v[0:7], v[40:47], v[128:131]
	v_mfma_f32_16x16x128_f8f6f4 v[120:123], v[8:15], v[48:55], v[120:123]
	v_mfma_f32_16x16x128_f8f6f4 v[112:115], v[0:7], v[48:55], v[112:115]
	v_mfma_f32_16x16x128_f8f6f4 v[104:107], v[8:15], v[56:63], v[104:107]
	v_mfma_f32_16x16x128_f8f6f4 v[96:99], v[0:7], v[56:63], v[96:99]
	v_mfma_f32_16x16x128_f8f6f4 v[88:91], v[8:15], v[240:247], v[88:91]
	v_mfma_f32_16x16x128_f8f6f4 v[80:83], v[0:7], v[240:247], v[80:83]
	s_setprio 0
	s_nop 0
	s_nop 0
	s_barrier
.Lpeel8_sub3:
	s_add_i32 s64, 0, 0x18000
	s_add_i32 s65, 0, 0x1c000
	v_add_u32_e32 v12, s64, v236
	v_add_u32_e32 v28, s65, v236
	ds_read_b128 v[0:3], v12
	ds_read_b128 v[4:7], v12 offset:1024
	ds_read_b128 v[8:11], v12 offset:2048
	ds_read_b128 v[12:15], v12 offset:3072
	ds_read_b128 v[16:19], v28
	ds_read_b128 v[20:23], v28 offset:1024
	ds_read_b128 v[24:27], v28 offset:2048
	ds_read_b128 v[28:31], v28 offset:3072
	s_mov_b32 m0, s45
	v_lshl_add_u64 v[248:249], s[36:37], 0, v[216:217]
	ds_read_b128 v[40:43], v237 offset:32768
	ds_read_b128 v[44:47], v237 offset:33792
	ds_read_b128 v[48:51], v237 offset:34816
	ds_read_b128 v[52:55], v237 offset:35840
	ds_read_b128 v[56:59], v237 offset:36864
	ds_read_b128 v[60:63], v237 offset:37888
	ds_read_b128 v[240:243], v237 offset:38912
	ds_read_b128 v[244:247], v237 offset:39936
	global_load_lds_dwordx4 v[248:249], off
	v_lshl_add_u64 v[248:249], s[36:37], 0, v[218:219]
	s_mov_b32 m0, s46
	s_nop 0
	global_load_lds_dwordx4 v[248:249], off
	s_waitcnt vmcnt(8)
	s_waitcnt lgkmcnt(0)
	s_barrier
	s_setprio 1
	s_waitcnt lgkmcnt(0)
	v_mfma_f32_16x16x128_f8f6f4 v[204:207], v[0:7], v[40:47], v[204:207]
	v_mfma_f32_16x16x128_f8f6f4 v[196:199], v[8:15], v[40:47], v[196:199]
	v_mfma_f32_16x16x128_f8f6f4 v[188:191], v[0:7], v[48:55], v[188:191]
	v_mfma_f32_16x16x128_f8f6f4 v[180:183], v[8:15], v[48:55], v[180:183]
	v_mfma_f32_16x16x128_f8f6f4 v[172:175], v[0:7], v[56:63], v[172:175]
	v_mfma_f32_16x16x128_f8f6f4 v[164:167], v[8:15], v[56:63], v[164:167]
	v_mfma_f32_16x16x128_f8f6f4 v[156:159], v[0:7], v[240:247], v[156:159]
	v_mfma_f32_16x16x128_f8f6f4 v[148:151], v[8:15], v[240:247], v[148:151]
	v_mfma_f32_16x16x128_f8f6f4 v[200:203], v[16:23], v[40:47], v[200:203]
	v_mfma_f32_16x16x128_f8f6f4 v[192:195], v[24:31], v[40:47], v[192:195]
	v_mfma_f32_16x16x128_f8f6f4 v[184:187], v[16:23], v[48:55], v[184:187]
	v_mfma_f32_16x16x128_f8f6f4 v[176:179], v[24:31], v[48:55], v[176:179]
	v_mfma_f32_16x16x128_f8f6f4 v[168:171], v[16:23], v[56:63], v[168:171]
	v_mfma_f32_16x16x128_f8f6f4 v[160:163], v[24:31], v[56:63], v[160:163]
	v_mfma_f32_16x16x128_f8f6f4 v[152:155], v[16:23], v[240:247], v[152:155]
	v_mfma_f32_16x16x128_f8f6f4 v[144:147], v[24:31], v[240:247], v[144:147]
	s_setprio 0
	s_nop 0
	s_nop 0
	s_barrier
	s_add_i32 s36, s64, s38
	v_lshl_add_u64 v[34:35], v[34:35], 0, s[12:13]
	s_mov_b32 m0, s36
	ds_read_b128 v[40:43], v237 offset:49152
	ds_read_b128 v[44:47], v237 offset:50176
	ds_read_b128 v[48:51], v237 offset:51200
	ds_read_b128 v[52:55], v237 offset:52224
	ds_read_b128 v[56:59], v237 offset:53248
	ds_read_b128 v[60:63], v237 offset:54272
	ds_read_b128 v[240:243], v237 offset:55296
	ds_read_b128 v[244:247], v237 offset:56320
	global_load_lds_dwordx4 v[34:35], off
	s_add_i32 m0, s36, 0x2000
	s_add_u32 s30, s30, 0x40080
	v_lshl_add_u64 v[32:33], v[32:33], 0, s[12:13]
	s_addc_u32 s31, s31, 0
	s_add_i32 s36, s65, s38
	global_load_lds_dwordx4 v[32:33], off
	v_lshl_add_u64 v[32:33], s[30:31], 0, v[208:209]
	s_mov_b32 m0, s36
	s_nop 0
	global_load_lds_dwordx4 v[32:33], off
	v_lshl_add_u64 v[32:33], s[30:31], 0, v[210:211]
	s_add_i32 m0, s36, 0x2000
	s_nop 0
	global_load_lds_dwordx4 v[32:33], off
	v_lshl_add_u64 v[32:33], v[38:39], 0, s[12:13]
	s_mov_b32 m0, s50
	s_nop 0
	global_load_lds_dwordx4 v[32:33], off
	v_lshl_add_u64 v[32:33], v[36:37], 0, s[12:13]
	s_mov_b32 m0, s51
	s_nop 0
	global_load_lds_dwordx4 v[32:33], off
	s_waitcnt vmcnt(8)
	s_waitcnt lgkmcnt(0)
	s_barrier
	s_setprio 1
	s_waitcnt lgkmcnt(0)
	v_mfma_f32_16x16x128_f8f6f4 v[140:143], v[0:7], v[40:47], v[140:143]
	v_mfma_f32_16x16x128_f8f6f4 v[132:135], v[8:15], v[40:47], v[132:135]
	v_mfma_f32_16x16x128_f8f6f4 v[124:127], v[0:7], v[48:55], v[124:127]
	v_mfma_f32_16x16x128_f8f6f4 v[116:119], v[8:15], v[48:55], v[116:119]
	v_mfma_f32_16x16x128_f8f6f4 v[108:111], v[0:7], v[56:63], v[108:111]
	v_mfma_f32_16x16x128_f8f6f4 v[100:103], v[8:15], v[56:63], v[100:103]
	v_mfma_f32_16x16x128_f8f6f4 v[92:95], v[0:7], v[240:247], v[92:95]
	v_mfma_f32_16x16x128_f8f6f4 v[84:87], v[8:15], v[240:247], v[84:87]
	v_mfma_f32_16x16x128_f8f6f4 v[136:139], v[16:23], v[40:47], v[136:139]
	v_mfma_f32_16x16x128_f8f6f4 v[128:131], v[24:31], v[40:47], v[128:131]
	v_mfma_f32_16x16x128_f8f6f4 v[120:123], v[16:23], v[48:55], v[120:123]
	v_mfma_f32_16x16x128_f8f6f4 v[112:115], v[24:31], v[48:55], v[112:115]
	v_mfma_f32_16x16x128_f8f6f4 v[104:107], v[16:23], v[56:63], v[104:107]
	v_mfma_f32_16x16x128_f8f6f4 v[96:99], v[24:31], v[56:63], v[96:99]
	v_mfma_f32_16x16x128_f8f6f4 v[88:91], v[16:23], v[240:247], v[88:91]
	v_mfma_f32_16x16x128_f8f6f4 v[80:83], v[24:31], v[240:247], v[80:83]
	s_setprio 0
	s_nop 0
	s_nop 0
	s_barrier
	s_add_i32 s63, s63, 2
	s_add_u32 s34, s34, 0x100
	s_addc_u32 s35, s35, 0
	s_add_u32 s23, s23, 0x100
	s_addc_u32 s29, s29, 0
	s_cmp_gt_u32 s63, 13
	s_cbranch_scc1 .LBB0_1194

.Lpeel9_cont:
	v_add_u32_e32 v0, s74, v186
	v_add_u32_e32 v12, s75, v186
	ds_read_b128 v[16:19], v0
	ds_read_b128 v[20:23], v0 offset:1024
	ds_read_b128 v[24:27], v0 offset:2048
	ds_read_b128 v[28:31], v0 offset:3072
	ds_read_b128 v[0:3], v12
	ds_read_b128 v[4:7], v12 offset:1024
	ds_read_b128 v[8:11], v12 offset:2048
	ds_read_b128 v[12:15], v12 offset:3072
	s_add_u32 s36, s44, 0xfffc0080
	s_addc_u32 s37, s45, -1
	s_and_b64 s[30:31], s[30:31], exec
	s_cselect_b32 s37, s29, s37
	s_cselect_b32 s36, s28, s36
	s_cselect_b32 s31, s41, s23
	s_cselect_b32 s30, s40, s21
	v_lshl_add_u64 v[214:215], s[44:45], 0, v[170:171]
	s_add_i32 m0, s62, 0xc000
	ds_read_b128 v[178:181], v187
	ds_read_b128 v[182:185], v187 offset:1024
	ds_read_b128 v[190:193], v187 offset:2048
	ds_read_b128 v[194:197], v187 offset:3072
	ds_read_b128 v[198:201], v187 offset:4096
	ds_read_b128 v[202:205], v187 offset:5120
	ds_read_b128 v[206:209], v187 offset:6144
	ds_read_b128 v[210:213], v187 offset:7168
	global_load_lds_dwordx4 v[214:215], off
	v_lshl_add_u64 v[214:215], s[44:45], 0, v[172:173]
	s_add_i32 m0, s62, 0xe000
	s_nop 0
	global_load_lds_dwordx4 v[214:215], off
	s_waitcnt vmcnt(8)
	s_waitcnt lgkmcnt(0)
	s_barrier
	s_setprio 1
	s_waitcnt lgkmcnt(0)
	v_mfma_f32_16x16x128_f8f6f4 v[156:159], v[16:23], v[178:185], 0
	v_mfma_f32_16x16x128_f8f6f4 v[152:155], v[24:31], v[178:185], 0
	v_mfma_f32_16x16x128_f8f6f4 v[140:143], v[16:23], v[190:197], 0
	v_mfma_f32_16x16x128_f8f6f4 v[136:139], v[24:31], v[190:197], 0
	v_mfma_f32_16x16x128_f8f6f4 v[124:127], v[16:23], v[198:205], 0
	v_mfma_f32_16x16x128_f8f6f4 v[120:123], v[24:31], v[198:205], 0
	v_mfma_f32_16x16x128_f8f6f4 v[108:111], v[16:23], v[206:213], 0
	v_mfma_f32_16x16x128_f8f6f4 v[104:107], v[24:31], v[206:213], 0
	v_mfma_f32_16x16x128_f8f6f4 v[148:151], v[0:7], v[178:185], 0
	v_mfma_f32_16x16x128_f8f6f4 v[144:147], v[8:15], v[178:185], 0
	v_mfma_f32_16x16x128_f8f6f4 v[132:135], v[0:7], v[190:197], 0
	v_mfma_f32_16x16x128_f8f6f4 v[128:131], v[8:15], v[190:197], 0
	v_mfma_f32_16x16x128_f8f6f4 v[116:119], v[0:7], v[198:205], 0
	v_mfma_f32_16x16x128_f8f6f4 v[112:115], v[8:15], v[198:205], 0
	v_mfma_f32_16x16x128_f8f6f4 v[100:103], v[0:7], v[206:213], 0
	v_mfma_f32_16x16x128_f8f6f4 v[96:99], v[8:15], v[206:213], 0
	s_setprio 0
	s_nop 0
	s_nop 0
	s_barrier
	s_add_i32 s38, s74, s47
	v_lshl_add_u64 v[178:179], s[30:31], 0, v[164:165]
	s_mov_b32 m0, s38
	ds_read_b128 v[190:193], v187 offset:16384
	ds_read_b128 v[194:197], v187 offset:17408
	ds_read_b128 v[198:201], v187 offset:18432
	ds_read_b128 v[202:205], v187 offset:19456
	ds_read_b128 v[206:209], v187 offset:20480
	ds_read_b128 v[210:213], v187 offset:21504
	ds_read_b128 v[214:217], v187 offset:22528
	ds_read_b128 v[218:221], v187 offset:23552
	global_load_lds_dwordx4 v[178:179], off
	s_add_i32 m0, s38, 0x2000
	s_add_u32 s38, s30, 0x40000
	v_lshl_add_u64 v[180:181], s[30:31], 0, v[168:169]
	s_addc_u32 s39, s31, 0
	s_add_i32 s43, s75, s47
	global_load_lds_dwordx4 v[180:181], off
	v_lshl_add_u64 v[182:183], s[38:39], 0, v[164:165]
	s_mov_b32 m0, s43
	v_lshl_add_u64 v[184:185], s[36:37], 0, v[166:167]
	global_load_lds_dwordx4 v[182:183], off
	v_lshl_add_u64 v[182:183], s[38:39], 0, v[168:169]
	s_add_i32 m0, s43, 0x2000
	s_nop 0
	global_load_lds_dwordx4 v[182:183], off
	v_lshl_add_u64 v[182:183], s[36:37], 0, v[162:163]
	s_mov_b32 m0, s62
	s_nop 0
	global_load_lds_dwordx4 v[182:183], off
	s_mov_b32 m0, s63
	s_nop 0
	global_load_lds_dwordx4 v[184:185], off
	s_waitcnt vmcnt(8)
	s_waitcnt lgkmcnt(0)
	s_barrier
	s_setprio 1
	s_waitcnt lgkmcnt(0)
	v_mfma_f32_16x16x128_f8f6f4 v[92:95], v[16:23], v[190:197], 0
	v_mfma_f32_16x16x128_f8f6f4 v[88:91], v[24:31], v[190:197], 0
	v_mfma_f32_16x16x128_f8f6f4 v[76:79], v[16:23], v[198:205], 0
	v_mfma_f32_16x16x128_f8f6f4 v[72:75], v[24:31], v[198:205], 0
	v_mfma_f32_16x16x128_f8f6f4 v[60:63], v[16:23], v[206:213], 0
	v_mfma_f32_16x16x128_f8f6f4 v[56:59], v[24:31], v[206:213], 0
	v_mfma_f32_16x16x128_f8f6f4 v[44:47], v[16:23], v[214:221], 0
	v_mfma_f32_16x16x128_f8f6f4 v[40:43], v[24:31], v[214:221], 0
	v_mfma_f32_16x16x128_f8f6f4 v[84:87], v[0:7], v[190:197], 0
	v_mfma_f32_16x16x128_f8f6f4 v[80:83], v[8:15], v[190:197], 0
	v_mfma_f32_16x16x128_f8f6f4 v[68:71], v[0:7], v[198:205], 0
	v_mfma_f32_16x16x128_f8f6f4 v[64:67], v[8:15], v[198:205], 0
	v_mfma_f32_16x16x128_f8f6f4 v[52:55], v[0:7], v[206:213], 0
	v_mfma_f32_16x16x128_f8f6f4 v[48:51], v[8:15], v[206:213], 0
	v_mfma_f32_16x16x128_f8f6f4 v[36:39], v[0:7], v[214:221], 0
	v_mfma_f32_16x16x128_f8f6f4 v[32:35], v[8:15], v[214:221], 0
	s_setprio 0
	s_nop 0
	s_nop 0
	s_barrier
	s_branch .Lpeel9_sub3
.LBB0_1270:
	v_add_u32_e32 v0, s74, v186
	v_add_u32_e32 v12, s75, v186
	ds_read_b128 v[16:19], v0
	ds_read_b128 v[20:23], v0 offset:1024
	ds_read_b128 v[24:27], v0 offset:2048
	ds_read_b128 v[28:31], v0 offset:3072
	ds_read_b128 v[0:3], v12
	ds_read_b128 v[4:7], v12 offset:1024
	ds_read_b128 v[8:11], v12 offset:2048
	ds_read_b128 v[12:15], v12 offset:3072
	s_add_u32 s36, s44, 0xfffc0080
	s_addc_u32 s37, s45, -1
	s_and_b64 s[30:31], s[30:31], exec
	s_cselect_b32 s37, s29, s37
	s_cselect_b32 s36, s28, s36
	s_cselect_b32 s31, s41, s23
	s_cselect_b32 s30, s40, s21
	v_lshl_add_u64 v[214:215], s[44:45], 0, v[170:171]
	s_add_i32 m0, s62, 0xc000
	ds_read_b128 v[178:181], v187
	ds_read_b128 v[182:185], v187 offset:1024
	ds_read_b128 v[190:193], v187 offset:2048
	ds_read_b128 v[194:197], v187 offset:3072
	ds_read_b128 v[198:201], v187 offset:4096
	ds_read_b128 v[202:205], v187 offset:5120
	ds_read_b128 v[206:209], v187 offset:6144
	ds_read_b128 v[210:213], v187 offset:7168
	global_load_lds_dwordx4 v[214:215], off
	v_lshl_add_u64 v[214:215], s[44:45], 0, v[172:173]
	s_add_i32 m0, s62, 0xe000
	s_nop 0
	global_load_lds_dwordx4 v[214:215], off
	s_waitcnt vmcnt(8)
	s_waitcnt lgkmcnt(0)
	s_barrier
	s_setprio 1
	s_waitcnt lgkmcnt(0)
	v_mfma_f32_16x16x128_f8f6f4 v[156:159], v[16:23], v[178:185], v[156:159]
	v_mfma_f32_16x16x128_f8f6f4 v[152:155], v[24:31], v[178:185], v[152:155]
	v_mfma_f32_16x16x128_f8f6f4 v[140:143], v[16:23], v[190:197], v[140:143]
	v_mfma_f32_16x16x128_f8f6f4 v[136:139], v[24:31], v[190:197], v[136:139]
	v_mfma_f32_16x16x128_f8f6f4 v[124:127], v[16:23], v[198:205], v[124:127]
	v_mfma_f32_16x16x128_f8f6f4 v[120:123], v[24:31], v[198:205], v[120:123]
	v_mfma_f32_16x16x128_f8f6f4 v[108:111], v[16:23], v[206:213], v[108:111]
	v_mfma_f32_16x16x128_f8f6f4 v[104:107], v[24:31], v[206:213], v[104:107]
	v_mfma_f32_16x16x128_f8f6f4 v[148:151], v[0:7], v[178:185], v[148:151]
	v_mfma_f32_16x16x128_f8f6f4 v[144:147], v[8:15], v[178:185], v[144:147]
	v_mfma_f32_16x16x128_f8f6f4 v[132:135], v[0:7], v[190:197], v[132:135]
	v_mfma_f32_16x16x128_f8f6f4 v[128:131], v[8:15], v[190:197], v[128:131]
	v_mfma_f32_16x16x128_f8f6f4 v[116:119], v[0:7], v[198:205], v[116:119]
	v_mfma_f32_16x16x128_f8f6f4 v[112:115], v[8:15], v[198:205], v[112:115]
	v_mfma_f32_16x16x128_f8f6f4 v[100:103], v[0:7], v[206:213], v[100:103]
	v_mfma_f32_16x16x128_f8f6f4 v[96:99], v[8:15], v[206:213], v[96:99]
	s_setprio 0
	s_nop 0
	s_nop 0
	s_barrier
	s_add_i32 s38, s74, s47
	v_lshl_add_u64 v[178:179], s[30:31], 0, v[164:165]
	s_mov_b32 m0, s38
	ds_read_b128 v[190:193], v187 offset:16384
	ds_read_b128 v[194:197], v187 offset:17408
	ds_read_b128 v[198:201], v187 offset:18432
	ds_read_b128 v[202:205], v187 offset:19456
	ds_read_b128 v[206:209], v187 offset:20480
	ds_read_b128 v[210:213], v187 offset:21504
	ds_read_b128 v[214:217], v187 offset:22528
	ds_read_b128 v[218:221], v187 offset:23552
	global_load_lds_dwordx4 v[178:179], off
	s_add_i32 m0, s38, 0x2000
	s_add_u32 s38, s30, 0x40000
	v_lshl_add_u64 v[180:181], s[30:31], 0, v[168:169]
	s_addc_u32 s39, s31, 0
	s_add_i32 s43, s75, s47
	global_load_lds_dwordx4 v[180:181], off
	v_lshl_add_u64 v[182:183], s[38:39], 0, v[164:165]
	s_mov_b32 m0, s43
	v_lshl_add_u64 v[184:185], s[36:37], 0, v[166:167]
	global_load_lds_dwordx4 v[182:183], off
	v_lshl_add_u64 v[182:183], s[38:39], 0, v[168:169]
	s_add_i32 m0, s43, 0x2000
	s_nop 0
	global_load_lds_dwordx4 v[182:183], off
	v_lshl_add_u64 v[182:183], s[36:37], 0, v[162:163]
	s_mov_b32 m0, s62
	s_nop 0
	global_load_lds_dwordx4 v[182:183], off
	s_mov_b32 m0, s63
	s_nop 0
	global_load_lds_dwordx4 v[184:185], off
	s_waitcnt vmcnt(8)
	s_waitcnt lgkmcnt(0)
	s_barrier
	s_setprio 1
	s_waitcnt lgkmcnt(0)
	v_mfma_f32_16x16x128_f8f6f4 v[92:95], v[16:23], v[190:197], v[92:95]
	v_mfma_f32_16x16x128_f8f6f4 v[88:91], v[24:31], v[190:197], v[88:91]
	v_mfma_f32_16x16x128_f8f6f4 v[76:79], v[16:23], v[198:205], v[76:79]
	v_mfma_f32_16x16x128_f8f6f4 v[72:75], v[24:31], v[198:205], v[72:75]
	v_mfma_f32_16x16x128_f8f6f4 v[60:63], v[16:23], v[206:213], v[60:63]
	v_mfma_f32_16x16x128_f8f6f4 v[56:59], v[24:31], v[206:213], v[56:59]
	v_mfma_f32_16x16x128_f8f6f4 v[44:47], v[16:23], v[214:221], v[44:47]
	v_mfma_f32_16x16x128_f8f6f4 v[40:43], v[24:31], v[214:221], v[40:43]
	v_mfma_f32_16x16x128_f8f6f4 v[84:87], v[0:7], v[190:197], v[84:87]
	v_mfma_f32_16x16x128_f8f6f4 v[80:83], v[8:15], v[190:197], v[80:83]
	v_mfma_f32_16x16x128_f8f6f4 v[68:71], v[0:7], v[198:205], v[68:71]
	v_mfma_f32_16x16x128_f8f6f4 v[64:67], v[8:15], v[198:205], v[64:67]
	v_mfma_f32_16x16x128_f8f6f4 v[52:55], v[0:7], v[206:213], v[52:55]
	v_mfma_f32_16x16x128_f8f6f4 v[48:51], v[8:15], v[206:213], v[48:51]
	v_mfma_f32_16x16x128_f8f6f4 v[36:39], v[0:7], v[214:221], v[36:39]
	v_mfma_f32_16x16x128_f8f6f4 v[32:35], v[8:15], v[214:221], v[32:35]
	s_setprio 0
	s_nop 0
	s_nop 0
	s_barrier
.Lpeel9_sub3:
	s_add_i32 s38, 0, 0x18000
	s_add_i32 s39, 0, 0x1c000
	v_add_u32_e32 v12, s38, v186
	v_add_u32_e32 v28, s39, v186
	ds_read_b128 v[0:3], v12
	ds_read_b128 v[4:7], v12 offset:1024
	ds_read_b128 v[8:11], v12 offset:2048
	ds_read_b128 v[12:15], v12 offset:3072
	ds_read_b128 v[16:19], v28
	ds_read_b128 v[20:23], v28 offset:1024
	ds_read_b128 v[24:27], v28 offset:2048
	ds_read_b128 v[28:31], v28 offset:3072
	s_add_u32 s36, s36, 0x40000
	s_addc_u32 s37, s37, 0
	s_mov_b32 m0, s64
	v_lshl_add_u64 v[222:223], s[36:37], 0, v[162:163]
	ds_read_b128 v[190:193], v187 offset:32768
	ds_read_b128 v[194:197], v187 offset:33792
	ds_read_b128 v[198:201], v187 offset:34816
	ds_read_b128 v[202:205], v187 offset:35840
	ds_read_b128 v[206:209], v187 offset:36864
	ds_read_b128 v[210:213], v187 offset:37888
	ds_read_b128 v[214:217], v187 offset:38912
	ds_read_b128 v[218:221], v187 offset:39936
	global_load_lds_dwordx4 v[222:223], off
	v_lshl_add_u64 v[222:223], s[36:37], 0, v[166:167]
	s_mov_b32 m0, s65
	s_nop 0
	global_load_lds_dwordx4 v[222:223], off
	s_waitcnt vmcnt(8)
	s_waitcnt lgkmcnt(0)
	s_barrier
	s_setprio 1
	s_waitcnt lgkmcnt(0)
	v_mfma_f32_16x16x128_f8f6f4 v[156:159], v[0:7], v[190:197], v[156:159]
	v_mfma_f32_16x16x128_f8f6f4 v[152:155], v[8:15], v[190:197], v[152:155]
	v_mfma_f32_16x16x128_f8f6f4 v[140:143], v[0:7], v[198:205], v[140:143]
	v_mfma_f32_16x16x128_f8f6f4 v[136:139], v[8:15], v[198:205], v[136:139]
	v_mfma_f32_16x16x128_f8f6f4 v[124:127], v[0:7], v[206:213], v[124:127]
	v_mfma_f32_16x16x128_f8f6f4 v[120:123], v[8:15], v[206:213], v[120:123]
	v_mfma_f32_16x16x128_f8f6f4 v[108:111], v[0:7], v[214:221], v[108:111]
	v_mfma_f32_16x16x128_f8f6f4 v[104:107], v[8:15], v[214:221], v[104:107]
	v_mfma_f32_16x16x128_f8f6f4 v[148:151], v[16:23], v[190:197], v[148:151]
	v_mfma_f32_16x16x128_f8f6f4 v[144:147], v[24:31], v[190:197], v[144:147]
	v_mfma_f32_16x16x128_f8f6f4 v[132:135], v[16:23], v[198:205], v[132:135]
	v_mfma_f32_16x16x128_f8f6f4 v[128:131], v[24:31], v[198:205], v[128:131]
	v_mfma_f32_16x16x128_f8f6f4 v[116:119], v[16:23], v[206:213], v[116:119]
	v_mfma_f32_16x16x128_f8f6f4 v[112:115], v[24:31], v[206:213], v[112:115]
	v_mfma_f32_16x16x128_f8f6f4 v[100:103], v[16:23], v[214:221], v[100:103]
	v_mfma_f32_16x16x128_f8f6f4 v[96:99], v[24:31], v[214:221], v[96:99]
	s_setprio 0
	s_nop 0
	s_nop 0
	s_barrier
	s_add_i32 s36, s38, s47
	v_lshl_add_u64 v[178:179], v[178:179], 0, s[14:15]
	s_mov_b32 m0, s36
	ds_read_b128 v[190:193], v187 offset:49152
	ds_read_b128 v[194:197], v187 offset:50176
	ds_read_b128 v[198:201], v187 offset:51200
	ds_read_b128 v[202:205], v187 offset:52224
	ds_read_b128 v[206:209], v187 offset:53248
	ds_read_b128 v[210:213], v187 offset:54272
	ds_read_b128 v[214:217], v187 offset:55296
	ds_read_b128 v[218:221], v187 offset:56320
	global_load_lds_dwordx4 v[178:179], off
	s_add_i32 m0, s36, 0x2000
	s_add_u32 s30, s30, 0x40080
	v_lshl_add_u64 v[178:179], v[180:181], 0, s[14:15]
	s_addc_u32 s31, s31, 0
	s_add_i32 s36, s39, s47
	global_load_lds_dwordx4 v[178:179], off
	v_lshl_add_u64 v[178:179], s[30:31], 0, v[164:165]
	s_mov_b32 m0, s36
	s_nop 0
	global_load_lds_dwordx4 v[178:179], off
	v_lshl_add_u64 v[178:179], s[30:31], 0, v[168:169]
	s_add_i32 m0, s36, 0x2000
	s_nop 0
	global_load_lds_dwordx4 v[178:179], off
	v_lshl_add_u64 v[178:179], v[182:183], 0, s[14:15]
	s_mov_b32 m0, s66
	s_nop 0
	global_load_lds_dwordx4 v[178:179], off
	v_lshl_add_u64 v[178:179], v[184:185], 0, s[14:15]
	s_mov_b32 m0, s67
	s_nop 0
	global_load_lds_dwordx4 v[178:179], off
	s_waitcnt vmcnt(8)
	s_waitcnt lgkmcnt(0)
	s_barrier
	s_setprio 1
	s_waitcnt lgkmcnt(0)
	v_mfma_f32_16x16x128_f8f6f4 v[92:95], v[0:7], v[190:197], v[92:95]
	v_mfma_f32_16x16x128_f8f6f4 v[88:91], v[8:15], v[190:197], v[88:91]
	v_mfma_f32_16x16x128_f8f6f4 v[76:79], v[0:7], v[198:205], v[76:79]
	v_mfma_f32_16x16x128_f8f6f4 v[72:75], v[8:15], v[198:205], v[72:75]
	v_mfma_f32_16x16x128_f8f6f4 v[60:63], v[0:7], v[206:213], v[60:63]
	v_mfma_f32_16x16x128_f8f6f4 v[56:59], v[8:15], v[206:213], v[56:59]
	v_mfma_f32_16x16x128_f8f6f4 v[44:47], v[0:7], v[214:221], v[44:47]
	v_mfma_f32_16x16x128_f8f6f4 v[40:43], v[8:15], v[214:221], v[40:43]
	v_mfma_f32_16x16x128_f8f6f4 v[84:87], v[16:23], v[190:197], v[84:87]
	v_mfma_f32_16x16x128_f8f6f4 v[80:83], v[24:31], v[190:197], v[80:83]
	v_mfma_f32_16x16x128_f8f6f4 v[68:71], v[16:23], v[198:205], v[68:71]
	v_mfma_f32_16x16x128_f8f6f4 v[64:67], v[24:31], v[198:205], v[64:67]
	v_mfma_f32_16x16x128_f8f6f4 v[52:55], v[16:23], v[206:213], v[52:55]
	v_mfma_f32_16x16x128_f8f6f4 v[48:51], v[24:31], v[206:213], v[48:51]
	v_mfma_f32_16x16x128_f8f6f4 v[36:39], v[16:23], v[214:221], v[36:39]
	v_mfma_f32_16x16x128_f8f6f4 v[32:35], v[24:31], v[214:221], v[32:35]
	s_setprio 0
	s_nop 0
	s_nop 0
	s_barrier
	s_add_i32 s35, s35, 2
	s_add_u32 s44, s44, 0x100
	s_addc_u32 s45, s45, 0
	s_add_u32 s21, s21, 0x100
	s_addc_u32 s23, s23, 0
	s_cmp_gt_u32 s35, 13
	s_cbranch_scc1 .LBB0_1273

.LBB0_1287:
	s_add_u32 s22, s16, s18
	v_add_u32_e32 v92, s35, v78
	v_add_u32_e32 v108, s36, v78
	s_addc_u32 s23, s17, s19
	ds_read_b128 v[80:83], v92
	ds_read_b128 v[84:87], v92 offset:1024
	ds_read_b128 v[88:91], v92 offset:2048
	ds_read_b128 v[92:95], v92 offset:3072
	ds_read_b128 v[96:99], v108
	ds_read_b128 v[100:103], v108 offset:1024
	ds_read_b128 v[104:107], v108 offset:2048
	ds_read_b128 v[108:111], v108 offset:3072
	s_add_u32 s43, s22, 0x78300100
	s_addc_u32 s44, s23, 0
	s_and_b64 s[22:23], s[20:21], exec
	s_cselect_b32 s23, s1, s44
	s_cselect_b32 s22, s0, s43
	s_add_u32 s43, s11, s18
	s_addc_u32 s44, s13, s19
	s_and_b64 s[20:21], s[20:21], exec
	s_cselect_b32 s21, s9, s44
	s_cselect_b32 s20, s8, s43
	s_mov_b32 m0, s37
	v_lshl_add_u64 v[144:145], v[74:75], 0, s[18:19]
	ds_read_b128 v[112:115], v79
	ds_read_b128 v[116:119], v79 offset:1024
	ds_read_b128 v[120:123], v79 offset:2048
	ds_read_b128 v[124:127], v79 offset:3072
	ds_read_b128 v[128:131], v79 offset:4096
	ds_read_b128 v[132:135], v79 offset:5120
	ds_read_b128 v[136:139], v79 offset:6144
	ds_read_b128 v[140:143], v79 offset:7168
	global_load_lds_dwordx4 v[144:145], off
	v_lshl_add_u64 v[144:145], v[76:77], 0, s[18:19]
	s_mov_b32 m0, s38
	s_nop 0
	global_load_lds_dwordx4 v[144:145], off
	s_waitcnt vmcnt(8)
	s_waitcnt lgkmcnt(0)
	s_barrier
	s_setprio 1
	s_waitcnt lgkmcnt(0)
	v_mfma_f32_16x16x128_f8f6f4 v[60:63], v[80:87], v[112:119], v[60:63]
	v_mfma_f32_16x16x128_f8f6f4 v[56:59], v[88:95], v[112:119], v[56:59]
	v_mfma_f32_16x16x128_f8f6f4 v[44:47], v[80:87], v[120:127], v[44:47]
	v_mfma_f32_16x16x128_f8f6f4 v[40:43], v[88:95], v[120:127], v[40:43]
	v_mfma_f32_16x16x128_f8f6f4 v[28:31], v[80:87], v[128:135], v[28:31]
	v_mfma_f32_16x16x128_f8f6f4 v[24:27], v[88:95], v[128:135], v[24:27]
	v_mfma_f32_16x16x128_f8f6f4 v[12:15], v[80:87], v[136:143], v[12:15]
	v_mfma_f32_16x16x128_f8f6f4 v[8:11], v[88:95], v[136:143], v[8:11]
	v_mfma_f32_16x16x128_f8f6f4 v[52:55], v[96:103], v[112:119], v[52:55]
	v_mfma_f32_16x16x128_f8f6f4 v[48:51], v[104:111], v[112:119], v[48:51]
	v_mfma_f32_16x16x128_f8f6f4 v[36:39], v[96:103], v[120:127], v[36:39]
	v_mfma_f32_16x16x128_f8f6f4 v[32:35], v[104:111], v[120:127], v[32:35]
	v_mfma_f32_16x16x128_f8f6f4 v[20:23], v[96:103], v[128:135], v[20:23]
	v_mfma_f32_16x16x128_f8f6f4 v[16:19], v[104:111], v[128:135], v[16:19]
	v_mfma_f32_16x16x128_f8f6f4 v[4:7], v[96:103], v[136:143], v[4:7]
	v_mfma_f32_16x16x128_f8f6f4 v[0:3], v[104:111], v[136:143], v[0:3]
	s_setprio 0
	s_nop 0
	s_nop 0
	s_barrier
	s_mov_b32 m0, s39
	v_lshl_add_u64 v[144:145], s[20:21], 0, v[66:67]
	s_add_u32 s44, s20, 0x40000
	global_load_lds_dwordx4 v[144:145], off
	v_lshl_add_u64 v[146:147], s[20:21], 0, v[70:71]
	s_mov_b32 m0, s40
	s_addc_u32 s45, s21, 0
	global_load_lds_dwordx4 v[146:147], off
	v_lshl_add_u64 v[80:81], s[44:45], 0, v[66:67]
	s_mov_b32 m0, s41
	v_lshl_add_u64 v[148:149], s[22:23], 0, v[64:65]
	global_load_lds_dwordx4 v[80:81], off
	v_lshl_add_u64 v[80:81], s[44:45], 0, v[70:71]
	s_mov_b32 m0, s42
	v_lshl_add_u64 v[150:151], s[22:23], 0, v[68:69]
	global_load_lds_dwordx4 v[80:81], off
	s_mov_b32 m0, s25
	s_nop 0
	global_load_lds_dwordx4 v[148:149], off
	s_mov_b32 m0, s26
	s_nop 0
	global_load_lds_dwordx4 v[150:151], off
	s_waitcnt vmcnt(8)
	s_waitcnt lgkmcnt(0)
	s_barrier
	s_barrier
	s_add_i32 s43, 0, 0x18000
	s_add_i32 s44, 0, 0x1c000
	v_add_u32_e32 v92, s43, v78
	v_add_u32_e32 v108, s44, v78
	ds_read_b128 v[80:83], v92
	ds_read_b128 v[84:87], v92 offset:1024
	ds_read_b128 v[88:91], v92 offset:2048
	ds_read_b128 v[92:95], v92 offset:3072
	ds_read_b128 v[96:99], v108
	ds_read_b128 v[100:103], v108 offset:1024
	ds_read_b128 v[104:107], v108 offset:2048
	ds_read_b128 v[108:111], v108 offset:3072
	s_add_u32 s22, s22, 0x40000
	s_addc_u32 s23, s23, 0
	s_mov_b32 m0, s27
	v_lshl_add_u64 v[152:153], s[22:23], 0, v[64:65]
	ds_read_b128 v[112:115], v79 offset:32768
	ds_read_b128 v[116:119], v79 offset:33792
	ds_read_b128 v[120:123], v79 offset:34816
	ds_read_b128 v[124:127], v79 offset:35840
	ds_read_b128 v[128:131], v79 offset:36864
	ds_read_b128 v[132:135], v79 offset:37888
	ds_read_b128 v[136:139], v79 offset:38912
	ds_read_b128 v[140:143], v79 offset:39936
	global_load_lds_dwordx4 v[152:153], off
	v_lshl_add_u64 v[152:153], s[22:23], 0, v[68:69]
	s_mov_b32 m0, s28
	s_nop 0
	global_load_lds_dwordx4 v[152:153], off
	s_waitcnt vmcnt(8)
	s_waitcnt lgkmcnt(0)
	s_barrier
	s_setprio 1
	s_waitcnt lgkmcnt(0)
	v_mfma_f32_16x16x128_f8f6f4 v[60:63], v[80:87], v[112:119], v[60:63]
	v_mfma_f32_16x16x128_f8f6f4 v[56:59], v[88:95], v[112:119], v[56:59]
	v_mfma_f32_16x16x128_f8f6f4 v[44:47], v[80:87], v[120:127], v[44:47]
	v_mfma_f32_16x16x128_f8f6f4 v[40:43], v[88:95], v[120:127], v[40:43]
	v_mfma_f32_16x16x128_f8f6f4 v[28:31], v[80:87], v[128:135], v[28:31]
	v_mfma_f32_16x16x128_f8f6f4 v[24:27], v[88:95], v[128:135], v[24:27]
	v_mfma_f32_16x16x128_f8f6f4 v[12:15], v[80:87], v[136:143], v[12:15]
	v_mfma_f32_16x16x128_f8f6f4 v[8:11], v[88:95], v[136:143], v[8:11]
	v_mfma_f32_16x16x128_f8f6f4 v[52:55], v[96:103], v[112:119], v[52:55]
	v_mfma_f32_16x16x128_f8f6f4 v[48:51], v[104:111], v[112:119], v[48:51]
	v_mfma_f32_16x16x128_f8f6f4 v[36:39], v[96:103], v[120:127], v[36:39]
	v_mfma_f32_16x16x128_f8f6f4 v[32:35], v[104:111], v[120:127], v[32:35]
	v_mfma_f32_16x16x128_f8f6f4 v[20:23], v[96:103], v[128:135], v[20:23]
	v_mfma_f32_16x16x128_f8f6f4 v[16:19], v[104:111], v[128:135], v[16:19]
	v_mfma_f32_16x16x128_f8f6f4 v[4:7], v[96:103], v[136:143], v[4:7]
	v_mfma_f32_16x16x128_f8f6f4 v[0:3], v[104:111], v[136:143], v[0:3]
	s_setprio 0
	s_nop 0
	s_nop 0
	s_barrier
	s_add_i32 s22, s43, s47
	v_lshl_add_u64 v[80:81], v[144:145], 0, s[14:15]
	s_mov_b32 m0, s22
	s_nop 0
	global_load_lds_dwordx4 v[80:81], off
	s_add_i32 m0, s22, 0x2000
	s_add_u32 s20, s20, 0x40080
	v_lshl_add_u64 v[80:81], v[146:147], 0, s[14:15]
	s_addc_u32 s21, s21, 0
	s_add_i32 s22, s44, s47
	global_load_lds_dwordx4 v[80:81], off
	v_lshl_add_u64 v[80:81], s[20:21], 0, v[66:67]
	s_mov_b32 m0, s22
	s_nop 0
	global_load_lds_dwordx4 v[80:81], off
	v_lshl_add_u64 v[80:81], s[20:21], 0, v[70:71]
	s_add_i32 m0, s22, 0x2000
	s_nop 0
	global_load_lds_dwordx4 v[80:81], off
	v_lshl_add_u64 v[80:81], v[148:149], 0, s[14:15]
	s_mov_b32 m0, s29
	s_nop 0
	global_load_lds_dwordx4 v[80:81], off
	v_lshl_add_u64 v[80:81], v[150:151], 0, s[14:15]
	s_mov_b32 m0, s30
	s_nop 0
	global_load_lds_dwordx4 v[80:81], off
	s_waitcnt vmcnt(8)
	s_waitcnt lgkmcnt(0)
	s_barrier
	s_barrier
	s_add_i32 s31, s31, 2
	s_add_u32 s18, s18, 0x100
	s_addc_u32 s19, s19, 0
	s_cmp_gt_u32 s31, 13
	s_cbranch_scc1 .LBB0_1290
